# hot loop heads (GEMM K-loops, first-trip copies, attention loop) aligned to 64 bytes instead of 8
# baseline (speedup 1.0000x reference)
.LBB0_125:
	s_mov_b32 s9, -2
	s_mov_b64 s[4:5], 0
	s_waitcnt vmcnt(8)
	.p2align 6
	s_nop 0
	ds_read_b128 v[130:133], v219
	ds_read_b128 v[134:137], v219 offset:2048
	ds_read_b128 v[138:141], v220
	ds_read_b128 v[142:145], v220 offset:2048
	ds_read_b128 v[146:149], v221
	ds_read_b128 v[150:153], v221 offset:2048
	ds_read_b128 v[154:157], v222
	ds_read_b128 v[158:161], v222 offset:2048
	ds_read_b128 v[162:165], v223
	ds_read_b128 v[166:169], v223 offset:2048
	ds_read_b128 v[170:173], v224
	ds_read_b128 v[174:177], v224 offset:2048
	ds_read_b128 v[178:181], v223 offset:4096
	ds_read_b128 v[182:185], v223 offset:6144
	ds_read_b128 v[186:189], v224 offset:4096
	ds_read_b128 v[190:193], v224 offset:6144
	s_add_u32 s47, s14, s4
	s_addc_u32 s50, s15, s5
	s_add_u32 s54, s47, 0x80
	s_addc_u32 s55, s50, 0
	s_mov_b32 m0, s70
	s_nop 0
	global_load_lds_dwordx4 v212, s[54:55] offset:0
	s_nop 0
	s_mov_b32 m0, s71
	s_nop 0
	global_load_lds_dwordx4 v214, s[54:55] offset:0
	s_waitcnt vmcnt(8)
	s_waitcnt lgkmcnt(0)
	s_barrier
	s_setprio 1
	s_waitcnt lgkmcnt(7)
	v_mfma_f32_16x16x32_bf16 v[126:129], v[130:133], v[162:165], 0
	v_mfma_f32_16x16x32_bf16 v[122:125], v[134:137], v[162:165], 0
	s_waitcnt lgkmcnt(6)
	v_mfma_f32_16x16x32_bf16 v[118:121], v[130:133], v[166:169], 0
	v_mfma_f32_16x16x32_bf16 v[114:117], v[134:137], v[166:169], 0
	s_waitcnt lgkmcnt(3)
	v_mfma_f32_16x16x32_bf16 v[110:113], v[130:133], v[178:181], 0
	v_mfma_f32_16x16x32_bf16 v[106:109], v[134:137], v[178:181], 0
	s_waitcnt lgkmcnt(2)
	v_mfma_f32_16x16x32_bf16 v[102:105], v[130:133], v[182:185], 0
	v_mfma_f32_16x16x32_bf16 v[98:101], v[134:137], v[182:185], 0
	v_mfma_f32_16x16x32_bf16 v[126:129], v[138:141], v[170:173], v[126:129]
	v_mfma_f32_16x16x32_bf16 v[122:125], v[142:145], v[170:173], v[122:125]
	v_mfma_f32_16x16x32_bf16 v[118:121], v[138:141], v[174:177], v[118:121]
	v_mfma_f32_16x16x32_bf16 v[114:117], v[142:145], v[174:177], v[114:117]
	s_waitcnt lgkmcnt(1)
	v_mfma_f32_16x16x32_bf16 v[110:113], v[138:141], v[186:189], v[110:113]
	v_mfma_f32_16x16x32_bf16 v[106:109], v[142:145], v[186:189], v[106:109]
	s_waitcnt lgkmcnt(0)
	v_mfma_f32_16x16x32_bf16 v[102:105], v[138:141], v[190:193], v[102:105]
	v_mfma_f32_16x16x32_bf16 v[98:101], v[142:145], v[190:193], v[98:101]
	s_setprio 0
	s_setprio 1
	v_mfma_f32_16x16x32_bf16 v[94:97], v[146:149], v[162:165], 0
	v_mfma_f32_16x16x32_bf16 v[90:93], v[150:153], v[162:165], 0
	v_mfma_f32_16x16x32_bf16 v[86:89], v[146:149], v[166:169], 0
	v_mfma_f32_16x16x32_bf16 v[82:85], v[150:153], v[166:169], 0
	v_mfma_f32_16x16x32_bf16 v[78:81], v[146:149], v[178:181], 0
	v_mfma_f32_16x16x32_bf16 v[74:77], v[150:153], v[178:181], 0
	v_mfma_f32_16x16x32_bf16 v[70:73], v[146:149], v[182:185], 0
	v_mfma_f32_16x16x32_bf16 v[66:69], v[150:153], v[182:185], 0
	v_mfma_f32_16x16x32_bf16 v[94:97], v[154:157], v[170:173], v[94:97]
	v_mfma_f32_16x16x32_bf16 v[90:93], v[158:161], v[170:173], v[90:93]
	v_mfma_f32_16x16x32_bf16 v[86:89], v[154:157], v[174:177], v[86:89]
	v_mfma_f32_16x16x32_bf16 v[82:85], v[158:161], v[174:177], v[82:85]
	v_mfma_f32_16x16x32_bf16 v[78:81], v[154:157], v[186:189], v[78:81]
	v_mfma_f32_16x16x32_bf16 v[74:77], v[158:161], v[186:189], v[74:77]
	v_mfma_f32_16x16x32_bf16 v[70:73], v[154:157], v[190:193], v[70:73]
	v_mfma_f32_16x16x32_bf16 v[66:69], v[158:161], v[190:193], v[66:69]
	s_setprio 0
	s_barrier
	s_add_u32 s51, s10, s4
	s_addc_u32 s53, s11, s5
	ds_read_b128 v[162:165], v223 offset:16384
	ds_read_b128 v[166:169], v223 offset:18432
	ds_read_b128 v[170:173], v224 offset:16384
	ds_read_b128 v[174:177], v224 offset:18432
	ds_read_b128 v[178:181], v223 offset:20480
	ds_read_b128 v[182:185], v223 offset:22528
	ds_read_b128 v[186:189], v224 offset:20480
	ds_read_b128 v[190:193], v224 offset:22528
	s_add_u32 s54, s51, 0x100
	s_addc_u32 s55, s53, 0
	s_mov_b32 m0, s57
	s_nop 0
	global_load_lds_dwordx4 v215, s[54:55] offset:0
	s_nop 0
	s_mov_b32 m0, s58
	s_nop 0
	global_load_lds_dwordx4 v216, s[54:55] offset:0
	s_add_u32 s54, s51, 0x40100
	s_addc_u32 s55, s53, 0
	s_mov_b32 m0, s59
	s_nop 0
	global_load_lds_dwordx4 v215, s[54:55] offset:0
	s_nop 0
	s_mov_b32 m0, s60
	s_nop 0
	global_load_lds_dwordx4 v216, s[54:55] offset:0
	s_add_u32 s54, s47, 0x100
	s_addc_u32 s55, s50, 0
	s_mov_b32 m0, s56
	s_nop 0
	global_load_lds_dwordx4 v211, s[54:55] offset:0
	s_nop 0
	s_mov_b32 m0, s61
	s_nop 0
	global_load_lds_dwordx4 v213, s[54:55] offset:0
	s_cmp_lg_u32 s9, 0xfffffffe
	s_cbranch_scc1 .Lrope_skip_ft
	s_lshl_b32 s100, s8, 14
	s_add_u32 s100, s96, s100
	s_addc_u32 s101, s97, 0
	s_mov_b32 m0, s98
	s_nop 0
	global_load_lds_dwordx4 v210, s[100:101] offset:0
	s_add_u32 s100, s100, 0x2000
	s_addc_u32 s101, s101, 0
	s_add_u32 s99, s98, 0x2000
	s_mov_b32 m0, s99
	s_nop 0
	global_load_lds_dwordx4 v210, s[100:101] offset:0

.LBB0_126:
	.p2align 6
	s_nop 0
	ds_read_b128 v[130:133], v219
	ds_read_b128 v[134:137], v219 offset:2048
	ds_read_b128 v[138:141], v220
	ds_read_b128 v[142:145], v220 offset:2048
	ds_read_b128 v[146:149], v221
	ds_read_b128 v[150:153], v221 offset:2048
	ds_read_b128 v[154:157], v222
	ds_read_b128 v[158:161], v222 offset:2048
	ds_read_b128 v[162:165], v223
	ds_read_b128 v[166:169], v223 offset:2048
	ds_read_b128 v[170:173], v224
	ds_read_b128 v[174:177], v224 offset:2048
	ds_read_b128 v[178:181], v223 offset:4096
	ds_read_b128 v[182:185], v223 offset:6144
	ds_read_b128 v[186:189], v224 offset:4096
	ds_read_b128 v[190:193], v224 offset:6144
	s_add_u32 s47, s14, s4
	s_addc_u32 s50, s15, s5
	s_add_u32 s54, s47, 0x80
	s_addc_u32 s55, s50, 0
	s_mov_b32 m0, s70
	s_nop 0
	global_load_lds_dwordx4 v212, s[54:55] offset:0
	s_nop 0
	s_mov_b32 m0, s71
	s_nop 0
	global_load_lds_dwordx4 v214, s[54:55] offset:0
	s_waitcnt vmcnt(8)
	s_waitcnt lgkmcnt(0)
	s_barrier
	s_setprio 1
	s_waitcnt lgkmcnt(7)
	v_mfma_f32_16x16x32_bf16 v[126:129], v[130:133], v[162:165], v[126:129]
	v_mfma_f32_16x16x32_bf16 v[122:125], v[134:137], v[162:165], v[122:125]
	s_waitcnt lgkmcnt(6)
	v_mfma_f32_16x16x32_bf16 v[118:121], v[130:133], v[166:169], v[118:121]
	v_mfma_f32_16x16x32_bf16 v[114:117], v[134:137], v[166:169], v[114:117]
	s_waitcnt lgkmcnt(3)
	v_mfma_f32_16x16x32_bf16 v[110:113], v[130:133], v[178:181], v[110:113]
	v_mfma_f32_16x16x32_bf16 v[106:109], v[134:137], v[178:181], v[106:109]
	s_waitcnt lgkmcnt(2)
	v_mfma_f32_16x16x32_bf16 v[102:105], v[130:133], v[182:185], v[102:105]
	v_mfma_f32_16x16x32_bf16 v[98:101], v[134:137], v[182:185], v[98:101]
	v_mfma_f32_16x16x32_bf16 v[126:129], v[138:141], v[170:173], v[126:129]
	v_mfma_f32_16x16x32_bf16 v[122:125], v[142:145], v[170:173], v[122:125]
	v_mfma_f32_16x16x32_bf16 v[118:121], v[138:141], v[174:177], v[118:121]
	v_mfma_f32_16x16x32_bf16 v[114:117], v[142:145], v[174:177], v[114:117]
	s_waitcnt lgkmcnt(1)
	v_mfma_f32_16x16x32_bf16 v[110:113], v[138:141], v[186:189], v[110:113]
	v_mfma_f32_16x16x32_bf16 v[106:109], v[142:145], v[186:189], v[106:109]
	s_waitcnt lgkmcnt(0)
	v_mfma_f32_16x16x32_bf16 v[102:105], v[138:141], v[190:193], v[102:105]
	v_mfma_f32_16x16x32_bf16 v[98:101], v[142:145], v[190:193], v[98:101]
	s_setprio 0
	s_setprio 1
	v_mfma_f32_16x16x32_bf16 v[94:97], v[146:149], v[162:165], v[94:97]
	v_mfma_f32_16x16x32_bf16 v[90:93], v[150:153], v[162:165], v[90:93]
	v_mfma_f32_16x16x32_bf16 v[86:89], v[146:149], v[166:169], v[86:89]
	v_mfma_f32_16x16x32_bf16 v[82:85], v[150:153], v[166:169], v[82:85]
	v_mfma_f32_16x16x32_bf16 v[78:81], v[146:149], v[178:181], v[78:81]
	v_mfma_f32_16x16x32_bf16 v[74:77], v[150:153], v[178:181], v[74:77]
	v_mfma_f32_16x16x32_bf16 v[70:73], v[146:149], v[182:185], v[70:73]
	v_mfma_f32_16x16x32_bf16 v[66:69], v[150:153], v[182:185], v[66:69]
	v_mfma_f32_16x16x32_bf16 v[94:97], v[154:157], v[170:173], v[94:97]
	v_mfma_f32_16x16x32_bf16 v[90:93], v[158:161], v[170:173], v[90:93]
	v_mfma_f32_16x16x32_bf16 v[86:89], v[154:157], v[174:177], v[86:89]
	v_mfma_f32_16x16x32_bf16 v[82:85], v[158:161], v[174:177], v[82:85]
	v_mfma_f32_16x16x32_bf16 v[78:81], v[154:157], v[186:189], v[78:81]
	v_mfma_f32_16x16x32_bf16 v[74:77], v[158:161], v[186:189], v[74:77]
	v_mfma_f32_16x16x32_bf16 v[70:73], v[154:157], v[190:193], v[70:73]
	v_mfma_f32_16x16x32_bf16 v[66:69], v[158:161], v[190:193], v[66:69]
	s_setprio 0
	s_barrier
	s_add_u32 s51, s10, s4
	s_addc_u32 s53, s11, s5
	ds_read_b128 v[162:165], v223 offset:16384
	ds_read_b128 v[166:169], v223 offset:18432
	ds_read_b128 v[170:173], v224 offset:16384
	ds_read_b128 v[174:177], v224 offset:18432
	ds_read_b128 v[178:181], v223 offset:20480
	ds_read_b128 v[182:185], v223 offset:22528
	ds_read_b128 v[186:189], v224 offset:20480
	ds_read_b128 v[190:193], v224 offset:22528
	s_add_u32 s54, s51, 0x100
	s_addc_u32 s55, s53, 0
	s_mov_b32 m0, s57
	s_nop 0
	global_load_lds_dwordx4 v215, s[54:55] offset:0
	s_nop 0
	s_mov_b32 m0, s58
	s_nop 0
	global_load_lds_dwordx4 v216, s[54:55] offset:0
	s_add_u32 s54, s51, 0x40100
	s_addc_u32 s55, s53, 0
	s_mov_b32 m0, s59
	s_nop 0
	global_load_lds_dwordx4 v215, s[54:55] offset:0
	s_nop 0
	s_mov_b32 m0, s60
	s_nop 0
	global_load_lds_dwordx4 v216, s[54:55] offset:0
	s_add_u32 s54, s47, 0x100
	s_addc_u32 s55, s50, 0
	s_mov_b32 m0, s56
	s_nop 0
	global_load_lds_dwordx4 v211, s[54:55] offset:0
	s_nop 0
	s_mov_b32 m0, s61
	s_nop 0
	global_load_lds_dwordx4 v213, s[54:55] offset:0
	s_cmp_lg_u32 s9, 0xfffffffe
	s_cbranch_scc1 .Lrope_skip
	s_lshl_b32 s100, s8, 14
	s_add_u32 s100, s96, s100
	s_addc_u32 s101, s97, 0
	s_mov_b32 m0, s98
	s_nop 0
	global_load_lds_dwordx4 v210, s[100:101] offset:0
	s_add_u32 s100, s100, 0x2000
	s_addc_u32 s101, s101, 0
	s_add_u32 s99, s98, 0x2000
	s_mov_b32 m0, s99
	s_nop 0
	global_load_lds_dwordx4 v210, s[100:101] offset:0

.LBB0_251:
	.p2align 6
	s_nop 0
	s_add_u32 s72, s90, s70
	s_addc_u32 s73, s91, s71
	s_add_u32 s6, s72, 0x100000
	s_addc_u32 s7, s73, 0
	s_add_u32 s88, s92, s70
	s_addc_u32 s89, s93, s71
	s_mov_b32 m0, s85
	s_nop 0
	global_load_lds_dwordx4 v168, s[6:7] offset:0
	s_add_u32 s6, s88, 0x100000
	s_addc_u32 s7, s89, 0
	s_mov_b32 m0, s86
	s_nop 0
	global_load_lds_dwordx4 v169, s[6:7] offset:0
	s_nop 0
	s_mov_b32 m0, s87
	s_nop 0
	global_load_lds_dwordx4 v170, s[6:7] offset:0
	ds_read_b128 v[66:69], v175
	ds_read_b128 v[82:85], v175 offset:4096
	ds_read_b128 v[114:117], v176
	ds_read_b128 v[184:187], v176 offset:4096
	ds_read_b128 v[196:199], v177
	ds_read_b128 v[200:203], v177 offset:4096
	ds_read_b128 v[204:207], v178
	ds_read_b128 v[208:211], v178 offset:4096
	s_waitcnt lgkmcnt(7)
	v_mfma_f32_32x32x16_bf16 v[66:81], v[66:69], v[110:113], 0
	v_exp_f32_e32 v120, v154
	v_exp_f32_e32 v121, v155
	v_exp_f32_e32 v152, v152
	v_exp_f32_e32 v153, v153
	v_exp_f32_e32 v150, v150
	v_exp_f32_e32 v151, v151
	v_exp_f32_e32 v148, v148
	s_waitcnt lgkmcnt(6)
	v_mfma_f32_32x32x16_bf16 v[82:97], v[82:85], v[110:113], 0
	v_exp_f32_e32 v149, v149
	v_exp_f32_e32 v146, v146
	v_exp_f32_e32 v147, v147
	v_exp_f32_e32 v144, v144
	v_exp_f32_e32 v145, v145
	v_exp_f32_e32 v154, v140
	v_exp_f32_e32 v155, v141
	s_waitcnt lgkmcnt(5)
	v_mfma_f32_32x32x16_bf16 v[66:81], v[114:117], v[106:109], v[66:81]
	v_exp_f32_e32 v116, v142
	v_exp_f32_e32 v117, v143
	v_pk_add_f32 v[114:115], v[126:127], v[144:145]
	v_pk_add_f32 v[140:141], v[134:135], v[152:153]
	v_pk_add_f32 v[142:143], v[122:123], v[154:155]
	v_pk_add_f32 v[212:213], v[136:137], v[120:121]
	v_pk_add_f32 v[214:215], v[124:125], v[116:117]
	s_waitcnt lgkmcnt(4)
	v_mfma_f32_32x32x16_bf16 v[82:97], v[184:187], v[106:109], v[82:97]
	v_pk_add_f32 v[184:185], v[130:131], v[148:149]
	v_pk_add_f32 v[186:187], v[128:129], v[146:147]
	v_pk_add_f32 v[216:217], v[132:133], v[150:151]
	v_pk_add_f32 v[186:187], v[212:213], v[186:187]
	v_pk_add_f32 v[214:215], v[216:217], v[214:215]
	v_pk_add_f32 v[142:143], v[184:185], v[142:143]
	v_pk_add_f32 v[114:115], v[140:141], v[114:115]
	s_waitcnt lgkmcnt(3)
	v_mfma_f32_32x32x16_bf16 v[66:81], v[196:199], v[102:105], v[66:81]
	v_pk_add_f32 v[114:115], v[114:115], v[142:143]
	v_pk_add_f32 v[140:141], v[186:187], v[214:215]
	v_pk_add_f32 v[114:115], v[140:141], v[114:115]
	v_cvt_pk_bf16_f32 v140, v136, v137
	v_cvt_pk_bf16_f32 v141, v134, v135
	v_cvt_pk_bf16_f32 v142, v132, v133
	s_waitcnt lgkmcnt(2)
	v_mfma_f32_32x32x16_bf16 v[82:97], v[200:203], v[102:105], v[82:97]
	v_pk_add_f32 v[114:115], v[114:115], v[114:115] op_sel:[0,1] op_sel_hi:[1,0]
	v_cvt_pk_bf16_f32 v143, v130, v131
	v_cvt_pk_bf16_f32 v128, v128, v129
	v_cvt_pk_bf16_f32 v129, v126, v127
	v_cvt_pk_bf16_f32 v130, v124, v125
	v_cvt_pk_bf16_f32 v131, v122, v123
	s_nop 0
	v_mov_b32_e32 v115, v114
	s_waitcnt lgkmcnt(1)
	v_mfma_f32_32x32x16_bf16 v[66:81], v[204:207], v[98:101], v[66:81]
	v_permlane32_swap_b32_e32 v114, v115
	v_cvt_pk_bf16_f32 v120, v120, v121
	v_cvt_pk_bf16_f32 v121, v152, v153
	v_cvt_pk_bf16_f32 v122, v150, v151
	v_cvt_pk_bf16_f32 v123, v148, v149
	v_cvt_pk_bf16_f32 v124, v146, v147
	s_waitcnt lgkmcnt(0)
	v_mfma_f32_32x32x16_bf16 v[82:97], v[208:211], v[98:101], v[82:97]
	v_cvt_pk_bf16_f32 v125, v144, v145
	v_cvt_pk_bf16_f32 v126, v116, v117
	v_cvt_pk_bf16_f32 v127, v154, v155
	v_permlane32_swap_b32_e32 v140, v142
	v_permlane32_swap_b32_e32 v141, v143
	v_permlane32_swap_b32_e32 v128, v130
	v_permlane32_swap_b32_e32 v129, v131
	v_permlane32_swap_b32_e32 v120, v122
	v_permlane32_swap_b32_e32 v121, v123
	v_permlane32_swap_b32_e32 v124, v126
	v_permlane32_swap_b32_e32 v125, v127
	ds_read_b64_tr_b16 v[132:133], v166 offset:0x8000
	ds_read_b64_tr_b16 v[134:135], v166 offset:0x8800
	ds_read_b64_tr_b16 v[144:145], v166 offset:0x9000
	ds_read_b64_tr_b16 v[146:147], v166 offset:0x9800
	ds_read_b64_tr_b16 v[148:149], v166 offset:0xa000
	ds_read_b64_tr_b16 v[150:151], v166 offset:0xa800
	ds_read_b64_tr_b16 v[152:153], v166 offset:0xb000
	ds_read_b64_tr_b16 v[154:155], v166 offset:0xb800
	ds_read_b64_tr_b16 v[184:185], v166 offset:0x8200
	ds_read_b64_tr_b16 v[186:187], v166 offset:0x8a00
	ds_read_b64_tr_b16 v[196:197], v166 offset:0x9200
	ds_read_b64_tr_b16 v[198:199], v166 offset:0x9a00
	ds_read_b64_tr_b16 v[200:201], v166 offset:0xa200
	ds_read_b64_tr_b16 v[202:203], v166 offset:0xaa00
	ds_read_b64_tr_b16 v[204:205], v166 offset:0xb200
	ds_read_b64_tr_b16 v[206:207], v166 offset:0xba00
	s_waitcnt lgkmcnt(8)
	s_nop 0
	v_mfma_f32_32x32x16_bf16 v[18:33], v[140:143], v[132:135], v[18:33]
	v_mfma_f32_32x32x16_bf16 v[18:33], v[128:131], v[144:147], v[18:33]
	v_mfma_f32_32x32x16_bf16 v[18:33], v[120:123], v[148:151], v[18:33]
	v_mfma_f32_32x32x16_bf16 v[18:33], v[124:127], v[152:155], v[18:33]
	ds_read_b64_tr_b16 v[132:133], v166 offset:0x8400
	ds_read_b64_tr_b16 v[134:135], v166 offset:0x8c00
	ds_read_b64_tr_b16 v[144:145], v166 offset:0x9400
	ds_read_b64_tr_b16 v[146:147], v166 offset:0x9c00
	ds_read_b64_tr_b16 v[148:149], v166 offset:0xa400
	ds_read_b64_tr_b16 v[150:151], v166 offset:0xac00
	ds_read_b64_tr_b16 v[152:153], v166 offset:0xb400
	ds_read_b64_tr_b16 v[154:155], v166 offset:0xbc00
	s_waitcnt lgkmcnt(8)
	v_mfma_f32_32x32x16_bf16 v[34:49], v[140:143], v[184:187], v[34:49]
	v_mfma_f32_32x32x16_bf16 v[34:49], v[128:131], v[196:199], v[34:49]
	v_mfma_f32_32x32x16_bf16 v[34:49], v[120:123], v[200:203], v[34:49]
	v_mfma_f32_32x32x16_bf16 v[34:49], v[124:127], v[204:207], v[34:49]
	ds_read_b64_tr_b16 v[184:185], v166 offset:0x8600
	ds_read_b64_tr_b16 v[186:187], v166 offset:0x8e00
	ds_read_b64_tr_b16 v[196:197], v166 offset:0x9600
	ds_read_b64_tr_b16 v[198:199], v166 offset:0x9e00
	ds_read_b64_tr_b16 v[200:201], v166 offset:0xa600
	ds_read_b64_tr_b16 v[202:203], v166 offset:0xae00
	ds_read_b64_tr_b16 v[204:205], v166 offset:0xb600
	ds_read_b64_tr_b16 v[206:207], v166 offset:0xbe00
	s_waitcnt lgkmcnt(8)
	v_mfma_f32_32x32x16_bf16 v[50:65], v[140:143], v[132:135], v[50:65]
	v_mfma_f32_32x32x16_bf16 v[50:65], v[128:131], v[144:147], v[50:65]
	v_mfma_f32_32x32x16_bf16 v[50:65], v[120:123], v[148:151], v[50:65]
	v_mfma_f32_32x32x16_bf16 v[50:65], v[124:127], v[152:155], v[50:65]
	s_waitcnt lgkmcnt(0)
	v_mfma_f32_32x32x16_bf16 v[2:17], v[140:143], v[184:187], v[2:17]
	s_add_i32 s6, s95, 0xffffff40
	s_cmp_le_i32 s6, s77
	v_mfma_f32_32x32x16_bf16 v[2:17], v[128:131], v[196:199], v[2:17]
	v_mfma_f32_32x32x16_bf16 v[2:17], v[120:123], v[200:203], v[2:17]
	v_mfma_f32_32x32x16_bf16 v[2:17], v[124:127], v[204:207], v[2:17]
	s_cbranch_scc1 .LBB0_253
	v_cmp_gt_i32_e64 s[66:67], 26, v183
	v_cmp_gt_i32_e64 s[68:69], 27, v183
	v_cmp_gt_i32_e64 s[64:65], 25, v183
	s_and_b64 s[66:67], s[68:69], s[66:67]
	v_cmp_gt_i32_e64 s[62:63], 24, v183
	s_and_b64 s[64:65], s[66:67], s[64:65]
	v_cmp_gt_i32_e64 s[60:61], 19, v183
	s_and_b64 s[62:63], s[64:65], s[62:63]
	v_cmp_gt_i32_e64 s[58:59], 18, v183
	s_and_b64 s[60:61], s[62:63], s[60:61]
	v_cmp_gt_i32_e64 s[56:57], 17, v183
	s_and_b64 s[58:59], s[60:61], s[58:59]
	v_cmp_gt_i32_e64 s[54:55], 16, v183
	s_and_b64 s[56:57], s[58:59], s[56:57]
	v_cmp_gt_i32_e64 s[52:53], 11, v183
	s_and_b64 s[54:55], s[56:57], s[54:55]
	v_cmp_gt_i32_e64 s[50:51], 10, v183
	s_and_b64 s[52:53], s[54:55], s[52:53]
	v_cmp_gt_i32_e64 s[48:49], 9, v183
	s_and_b64 s[50:51], s[52:53], s[50:51]
	v_cmp_gt_i32_e64 s[44:45], 8, v183
	s_and_b64 s[48:49], s[50:51], s[48:49]
	v_cmp_gt_i32_e64 s[42:43], 3, v183
	s_and_b64 s[44:45], s[48:49], s[44:45]
	v_cmp_gt_i32_e64 s[40:41], 2, v183
	s_and_b64 s[42:43], s[44:45], s[42:43]
	v_cmp_gt_i32_e64 s[38:39], 1, v183
	s_and_b64 s[40:41], s[42:43], s[40:41]
	v_cmp_gt_i32_e64 s[36:37], 0, v183
	s_and_b64 s[38:39], s[40:41], s[38:39]
	s_and_b64 s[36:37], s[38:39], s[36:37]
	v_cmp_gt_i32_e64 s[34:35], 58, v183
	v_cndmask_b32_e64 v66, v66, v160, s[36:37]
	v_cmp_gt_i32_e64 s[36:37], 59, v183
	v_cmp_gt_i32_e64 s[30:31], 57, v183
	s_and_b64 s[34:35], s[36:37], s[34:35]
	v_cmp_gt_i32_e64 s[28:29], 56, v183
	s_and_b64 s[30:31], s[34:35], s[30:31]
	v_cmp_gt_i32_e64 s[26:27], 51, v183
	s_and_b64 s[28:29], s[30:31], s[28:29]
	v_cmp_gt_i32_e64 s[24:25], 50, v183
	s_and_b64 s[26:27], s[28:29], s[26:27]
	v_cmp_gt_i32_e64 s[22:23], 49, v183
	s_and_b64 s[24:25], s[26:27], s[24:25]
	v_cmp_gt_i32_e64 s[20:21], 48, v183
	s_and_b64 s[22:23], s[24:25], s[22:23]
	v_cmp_gt_i32_e64 s[18:19], 43, v183
	s_and_b64 s[20:21], s[22:23], s[20:21]
	v_cmp_gt_i32_e64 s[16:17], 42, v183
	s_and_b64 s[18:19], s[20:21], s[18:19]
	v_cmp_gt_i32_e64 s[14:15], 41, v183
	s_and_b64 s[16:17], s[18:19], s[16:17]
	v_cmp_gt_i32_e64 s[12:13], 40, v183
	s_and_b64 s[14:15], s[16:17], s[14:15]
	v_cmp_gt_i32_e64 s[10:11], 35, v183
	s_and_b64 s[12:13], s[14:15], s[12:13]
	v_cmp_gt_i32_e64 s[8:9], 34, v183
	s_and_b64 s[10:11], s[12:13], s[10:11]
	v_cmp_gt_i32_e64 s[6:7], 33, v183
	s_and_b64 s[8:9], s[10:11], s[8:9]
	v_cmp_gt_i32_e32 vcc, 32, v183
	s_and_b64 s[6:7], s[8:9], s[6:7]
	s_and_b64 vcc, s[6:7], vcc
	v_cndmask_b32_e64 v81, v81, v160, s[68:69]
	v_cndmask_b32_e64 v80, v80, v160, s[66:67]
	v_cndmask_b32_e64 v79, v79, v160, s[64:65]
	v_cndmask_b32_e64 v78, v78, v160, s[62:63]
	v_cndmask_b32_e64 v77, v77, v160, s[60:61]
	v_cndmask_b32_e64 v76, v76, v160, s[58:59]
	v_cndmask_b32_e64 v75, v75, v160, s[56:57]
	v_cndmask_b32_e64 v74, v74, v160, s[54:55]
	v_cndmask_b32_e64 v73, v73, v160, s[52:53]
	v_cndmask_b32_e64 v72, v72, v160, s[50:51]
	v_cndmask_b32_e64 v71, v71, v160, s[48:49]
	v_cndmask_b32_e64 v70, v70, v160, s[44:45]
	v_cndmask_b32_e64 v69, v69, v160, s[42:43]
	v_cndmask_b32_e64 v68, v68, v160, s[40:41]
	v_cndmask_b32_e64 v67, v67, v160, s[38:39]
	v_cndmask_b32_e64 v97, v97, v160, s[36:37]
	v_cndmask_b32_e64 v96, v96, v160, s[34:35]
	v_cndmask_b32_e64 v95, v95, v160, s[30:31]
	v_cndmask_b32_e64 v94, v94, v160, s[28:29]
	v_cndmask_b32_e64 v93, v93, v160, s[26:27]
	v_cndmask_b32_e64 v92, v92, v160, s[24:25]
	v_cndmask_b32_e64 v91, v91, v160, s[22:23]
	v_cndmask_b32_e64 v90, v90, v160, s[20:21]
	v_cndmask_b32_e64 v89, v89, v160, s[18:19]
	v_cndmask_b32_e64 v88, v88, v160, s[16:17]
	v_cndmask_b32_e64 v87, v87, v160, s[14:15]
	v_cndmask_b32_e64 v86, v86, v160, s[12:13]
	v_cndmask_b32_e64 v85, v85, v160, s[10:11]
	v_cndmask_b32_e64 v84, v84, v160, s[8:9]
	v_cndmask_b32_e64 v83, v83, v160, s[6:7]
	v_cndmask_b32_e32 v82, v82, v160, vcc

.LBB0_367:
	s_mov_b32 s31, -2
	s_mov_b64 s[6:7], 0
	.p2align 6
	s_nop 0
	ds_read_b128 v[130:133], v203
	ds_read_b128 v[134:137], v203 offset:2048
	ds_read_b128 v[138:141], v204
	ds_read_b128 v[142:145], v204 offset:2048
	ds_read_b128 v[146:149], v205
	ds_read_b128 v[150:153], v205 offset:2048
	ds_read_b128 v[154:157], v206
	ds_read_b128 v[158:161], v206 offset:2048
	ds_read_b128 v[162:165], v207
	ds_read_b128 v[166:169], v207 offset:2048
	ds_read_b128 v[174:177], v208
	ds_read_b128 v[178:181], v208 offset:2048
	ds_read_b128 v[182:185], v207 offset:4096
	ds_read_b128 v[210:213], v207 offset:6144
	ds_read_b128 v[214:217], v208 offset:4096
	ds_read_b128 v[218:221], v208 offset:6144
	s_add_u32 s36, s8, s6
	s_addc_u32 s37, s9, s7
	s_add_u32 s58, s36, 0x80
	s_addc_u32 s59, s37, 0
	s_mov_b32 m0, s52
	s_nop 0
	global_load_lds_dwordx4 v198, s[58:59] offset:0
	s_nop 0
	s_mov_b32 m0, s53
	s_nop 0
	global_load_lds_dwordx4 v200, s[58:59] offset:0
	s_waitcnt vmcnt(8)
	s_waitcnt lgkmcnt(0)
	s_barrier
	s_setprio 1
	s_waitcnt lgkmcnt(7)
	v_mfma_f32_16x16x32_bf16 v[126:129], v[130:133], v[162:165], 0
	v_mfma_f32_16x16x32_bf16 v[122:125], v[134:137], v[162:165], 0
	s_waitcnt lgkmcnt(6)
	v_mfma_f32_16x16x32_bf16 v[118:121], v[130:133], v[166:169], 0
	v_mfma_f32_16x16x32_bf16 v[114:117], v[134:137], v[166:169], 0
	s_waitcnt lgkmcnt(3)
	v_mfma_f32_16x16x32_bf16 v[110:113], v[130:133], v[182:185], 0
	v_mfma_f32_16x16x32_bf16 v[106:109], v[134:137], v[182:185], 0
	s_waitcnt lgkmcnt(2)
	v_mfma_f32_16x16x32_bf16 v[102:105], v[130:133], v[210:213], 0
	v_mfma_f32_16x16x32_bf16 v[98:101], v[134:137], v[210:213], 0
	v_mfma_f32_16x16x32_bf16 v[126:129], v[138:141], v[174:177], v[126:129]
	v_mfma_f32_16x16x32_bf16 v[122:125], v[142:145], v[174:177], v[122:125]
	v_mfma_f32_16x16x32_bf16 v[118:121], v[138:141], v[178:181], v[118:121]
	v_mfma_f32_16x16x32_bf16 v[114:117], v[142:145], v[178:181], v[114:117]
	s_waitcnt lgkmcnt(1)
	v_mfma_f32_16x16x32_bf16 v[110:113], v[138:141], v[214:217], v[110:113]
	v_mfma_f32_16x16x32_bf16 v[106:109], v[142:145], v[214:217], v[106:109]
	s_waitcnt lgkmcnt(0)
	v_mfma_f32_16x16x32_bf16 v[102:105], v[138:141], v[218:221], v[102:105]
	v_mfma_f32_16x16x32_bf16 v[98:101], v[142:145], v[218:221], v[98:101]
	s_setprio 0
	s_setprio 1
	v_mfma_f32_16x16x32_bf16 v[94:97], v[146:149], v[162:165], 0
	v_mfma_f32_16x16x32_bf16 v[90:93], v[150:153], v[162:165], 0
	v_mfma_f32_16x16x32_bf16 v[86:89], v[146:149], v[166:169], 0
	v_mfma_f32_16x16x32_bf16 v[82:85], v[150:153], v[166:169], 0
	v_mfma_f32_16x16x32_bf16 v[78:81], v[146:149], v[182:185], 0
	v_mfma_f32_16x16x32_bf16 v[74:77], v[150:153], v[182:185], 0
	v_mfma_f32_16x16x32_bf16 v[70:73], v[146:149], v[210:213], 0
	v_mfma_f32_16x16x32_bf16 v[66:69], v[150:153], v[210:213], 0
	v_mfma_f32_16x16x32_bf16 v[94:97], v[154:157], v[174:177], v[94:97]
	v_mfma_f32_16x16x32_bf16 v[90:93], v[158:161], v[174:177], v[90:93]
	v_mfma_f32_16x16x32_bf16 v[86:89], v[154:157], v[178:181], v[86:89]
	v_mfma_f32_16x16x32_bf16 v[82:85], v[158:161], v[178:181], v[82:85]
	v_mfma_f32_16x16x32_bf16 v[78:81], v[154:157], v[214:217], v[78:81]
	v_mfma_f32_16x16x32_bf16 v[74:77], v[158:161], v[214:217], v[74:77]
	v_mfma_f32_16x16x32_bf16 v[70:73], v[154:157], v[218:221], v[70:73]
	v_mfma_f32_16x16x32_bf16 v[66:69], v[158:161], v[218:221], v[66:69]
	s_setprio 0
	s_barrier
	s_add_u32 s60, s34, s6
	s_addc_u32 s61, s35, s7
	ds_read_b128 v[162:165], v207 offset:16384
	ds_read_b128 v[166:169], v207 offset:18432
	ds_read_b128 v[174:177], v208 offset:16384
	ds_read_b128 v[178:181], v208 offset:18432
	ds_read_b128 v[182:185], v207 offset:20480
	ds_read_b128 v[210:213], v207 offset:22528
	ds_read_b128 v[214:217], v208 offset:20480
	ds_read_b128 v[218:221], v208 offset:22528
	s_add_u32 s58, s60, 0x100
	s_addc_u32 s59, s61, 0
	s_mov_b32 m0, s39
	s_nop 0
	global_load_lds_dwordx4 v195, s[58:59] offset:0
	s_nop 0
	s_mov_b32 m0, s40
	s_nop 0
	global_load_lds_dwordx4 v196, s[58:59] offset:0
	s_add_u32 s58, s60, 0x40100
	s_addc_u32 s59, s61, 0
	s_mov_b32 m0, s41
	s_nop 0
	global_load_lds_dwordx4 v195, s[58:59] offset:0
	s_nop 0
	s_mov_b32 m0, s42
	s_nop 0
	global_load_lds_dwordx4 v196, s[58:59] offset:0
	s_add_u32 s58, s36, 0x100
	s_addc_u32 s59, s37, 0
	s_mov_b32 m0, s38
	s_nop 0
	global_load_lds_dwordx4 v197, s[58:59] offset:0
	s_nop 0
	s_mov_b32 m0, s43
	s_nop 0
	global_load_lds_dwordx4 v199, s[58:59] offset:0
	s_waitcnt vmcnt(8)
	s_waitcnt lgkmcnt(0)
	s_barrier
	s_setprio 1
	s_waitcnt lgkmcnt(7)
	v_mfma_f32_16x16x32_bf16 v[62:65], v[130:133], v[162:165], 0
	v_mfma_f32_16x16x32_bf16 v[58:61], v[134:137], v[162:165], 0
	s_waitcnt lgkmcnt(6)
	v_mfma_f32_16x16x32_bf16 v[54:57], v[130:133], v[166:169], 0
	v_mfma_f32_16x16x32_bf16 v[50:53], v[134:137], v[166:169], 0
	s_waitcnt lgkmcnt(3)
	v_mfma_f32_16x16x32_bf16 v[46:49], v[130:133], v[182:185], 0
	v_mfma_f32_16x16x32_bf16 v[42:45], v[134:137], v[182:185], 0
	s_waitcnt lgkmcnt(2)
	v_mfma_f32_16x16x32_bf16 v[38:41], v[130:133], v[210:213], 0
	v_mfma_f32_16x16x32_bf16 v[34:37], v[134:137], v[210:213], 0
	v_mfma_f32_16x16x32_bf16 v[62:65], v[138:141], v[174:177], v[62:65]
	v_mfma_f32_16x16x32_bf16 v[58:61], v[142:145], v[174:177], v[58:61]
	v_mfma_f32_16x16x32_bf16 v[54:57], v[138:141], v[178:181], v[54:57]
	v_mfma_f32_16x16x32_bf16 v[50:53], v[142:145], v[178:181], v[50:53]
	s_waitcnt lgkmcnt(1)
	v_mfma_f32_16x16x32_bf16 v[46:49], v[138:141], v[214:217], v[46:49]
	v_mfma_f32_16x16x32_bf16 v[42:45], v[142:145], v[214:217], v[42:45]
	s_waitcnt lgkmcnt(0)
	v_mfma_f32_16x16x32_bf16 v[38:41], v[138:141], v[218:221], v[38:41]
	v_mfma_f32_16x16x32_bf16 v[34:37], v[142:145], v[218:221], v[34:37]
	s_setprio 0
	s_setprio 1
	v_mfma_f32_16x16x32_bf16 v[30:33], v[146:149], v[162:165], 0
	v_mfma_f32_16x16x32_bf16 v[26:29], v[150:153], v[162:165], 0
	v_mfma_f32_16x16x32_bf16 v[22:25], v[146:149], v[166:169], 0
	v_mfma_f32_16x16x32_bf16 v[18:21], v[150:153], v[166:169], 0
	v_mfma_f32_16x16x32_bf16 v[14:17], v[146:149], v[182:185], 0
	v_mfma_f32_16x16x32_bf16 v[10:13], v[150:153], v[182:185], 0
	v_mfma_f32_16x16x32_bf16 v[6:9], v[146:149], v[210:213], 0
	v_mfma_f32_16x16x32_bf16 v[2:5], v[150:153], v[210:213], 0
	v_mfma_f32_16x16x32_bf16 v[30:33], v[154:157], v[174:177], v[30:33]
	v_mfma_f32_16x16x32_bf16 v[26:29], v[158:161], v[174:177], v[26:29]
	v_mfma_f32_16x16x32_bf16 v[22:25], v[154:157], v[178:181], v[22:25]
	v_mfma_f32_16x16x32_bf16 v[18:21], v[158:161], v[178:181], v[18:21]
	v_mfma_f32_16x16x32_bf16 v[14:17], v[154:157], v[214:217], v[14:17]
	v_mfma_f32_16x16x32_bf16 v[10:13], v[158:161], v[214:217], v[10:13]
	v_mfma_f32_16x16x32_bf16 v[6:9], v[154:157], v[218:221], v[6:9]
	v_mfma_f32_16x16x32_bf16 v[2:5], v[158:161], v[218:221], v[2:5]
	s_setprio 0
	s_barrier
	s_add_i32 s62, 0, 0x18000
	v_add_u32_e32 v174, s62, v201
	v_add_u32_e32 v175, s62, v202
	s_add_i32 s62, 0, 0x1c000
	v_add_u32_e32 v176, s62, v201
	ds_read_b128 v[130:133], v174
	ds_read_b128 v[134:137], v174 offset:2048
	ds_read_b128 v[138:141], v175
	ds_read_b128 v[142:145], v175 offset:2048
	v_add_u32_e32 v177, s62, v202
	ds_read_b128 v[146:149], v176
	ds_read_b128 v[150:153], v176 offset:2048
	ds_read_b128 v[154:157], v177
	ds_read_b128 v[158:161], v177 offset:2048
	ds_read_b128 v[162:165], v207 offset:32768
	ds_read_b128 v[166:169], v207 offset:34816
	ds_read_b128 v[178:181], v208 offset:32768
	ds_read_b128 v[182:185], v208 offset:34816
	ds_read_b128 v[210:213], v207 offset:36864
	ds_read_b128 v[214:217], v207 offset:38912
	ds_read_b128 v[218:221], v208 offset:36864
	ds_read_b128 v[222:225], v208 offset:38912
	s_mov_b32 m0, s44
	s_nop 0
	global_load_lds_dwordx4 v198, s[58:59] offset:0
	s_nop 0
	s_mov_b32 m0, s45
	s_nop 0
	global_load_lds_dwordx4 v200, s[58:59] offset:0
	s_waitcnt vmcnt(8)
	s_waitcnt lgkmcnt(0)
	s_barrier
	s_setprio 1
	s_waitcnt lgkmcnt(7)
	v_mfma_f32_16x16x32_bf16 v[126:129], v[130:133], v[162:165], v[126:129]
	v_mfma_f32_16x16x32_bf16 v[122:125], v[134:137], v[162:165], v[122:125]
	s_waitcnt lgkmcnt(6)
	v_mfma_f32_16x16x32_bf16 v[118:121], v[130:133], v[166:169], v[118:121]
	v_mfma_f32_16x16x32_bf16 v[114:117], v[134:137], v[166:169], v[114:117]
	s_waitcnt lgkmcnt(3)
	v_mfma_f32_16x16x32_bf16 v[110:113], v[130:133], v[210:213], v[110:113]
	v_mfma_f32_16x16x32_bf16 v[106:109], v[134:137], v[210:213], v[106:109]
	s_waitcnt lgkmcnt(2)
	v_mfma_f32_16x16x32_bf16 v[102:105], v[130:133], v[214:217], v[102:105]
	v_mfma_f32_16x16x32_bf16 v[98:101], v[134:137], v[214:217], v[98:101]
	v_mfma_f32_16x16x32_bf16 v[126:129], v[138:141], v[178:181], v[126:129]
	v_mfma_f32_16x16x32_bf16 v[122:125], v[142:145], v[178:181], v[122:125]
	v_mfma_f32_16x16x32_bf16 v[118:121], v[138:141], v[182:185], v[118:121]
	v_mfma_f32_16x16x32_bf16 v[114:117], v[142:145], v[182:185], v[114:117]
	s_waitcnt lgkmcnt(1)
	v_mfma_f32_16x16x32_bf16 v[110:113], v[138:141], v[218:221], v[110:113]
	v_mfma_f32_16x16x32_bf16 v[106:109], v[142:145], v[218:221], v[106:109]
	s_waitcnt lgkmcnt(0)
	v_mfma_f32_16x16x32_bf16 v[102:105], v[138:141], v[222:225], v[102:105]
	v_mfma_f32_16x16x32_bf16 v[98:101], v[142:145], v[222:225], v[98:101]
	s_setprio 0
	s_setprio 1
	v_mfma_f32_16x16x32_bf16 v[94:97], v[146:149], v[162:165], v[94:97]
	v_mfma_f32_16x16x32_bf16 v[90:93], v[150:153], v[162:165], v[90:93]
	v_mfma_f32_16x16x32_bf16 v[86:89], v[146:149], v[166:169], v[86:89]
	v_mfma_f32_16x16x32_bf16 v[82:85], v[150:153], v[166:169], v[82:85]
	v_mfma_f32_16x16x32_bf16 v[78:81], v[146:149], v[210:213], v[78:81]
	v_mfma_f32_16x16x32_bf16 v[74:77], v[150:153], v[210:213], v[74:77]
	v_mfma_f32_16x16x32_bf16 v[70:73], v[146:149], v[214:217], v[70:73]
	v_mfma_f32_16x16x32_bf16 v[66:69], v[150:153], v[214:217], v[66:69]
	v_mfma_f32_16x16x32_bf16 v[94:97], v[154:157], v[178:181], v[94:97]
	v_mfma_f32_16x16x32_bf16 v[90:93], v[158:161], v[178:181], v[90:93]
	v_mfma_f32_16x16x32_bf16 v[86:89], v[154:157], v[182:185], v[86:89]
	v_mfma_f32_16x16x32_bf16 v[82:85], v[158:161], v[182:185], v[82:85]
	v_mfma_f32_16x16x32_bf16 v[78:81], v[154:157], v[218:221], v[78:81]
	v_mfma_f32_16x16x32_bf16 v[74:77], v[158:161], v[218:221], v[74:77]
	v_mfma_f32_16x16x32_bf16 v[70:73], v[154:157], v[222:225], v[70:73]
	v_mfma_f32_16x16x32_bf16 v[66:69], v[158:161], v[222:225], v[66:69]
	s_setprio 0
	s_barrier
	ds_read_b128 v[162:165], v207 offset:49152
	ds_read_b128 v[166:169], v207 offset:51200
	ds_read_b128 v[178:181], v208 offset:49152
	ds_read_b128 v[182:185], v208 offset:51200
	ds_read_b128 v[210:213], v207 offset:53248
	ds_read_b128 v[214:217], v207 offset:55296
	ds_read_b128 v[218:221], v208 offset:53248
	ds_read_b128 v[222:225], v208 offset:55296
	s_add_u32 s58, s60, 0x180
	s_addc_u32 s59, s61, 0
	s_mov_b32 m0, s46
	s_nop 0
	global_load_lds_dwordx4 v195, s[58:59] offset:0
	s_nop 0
	s_mov_b32 m0, s47
	s_nop 0
	global_load_lds_dwordx4 v196, s[58:59] offset:0
	s_add_u32 s58, s60, 0x40180
	s_addc_u32 s59, s61, 0
	s_mov_b32 m0, s50
	s_nop 0
	global_load_lds_dwordx4 v195, s[58:59] offset:0
	s_add_u32 s36, s36, 0x180
	s_mov_b32 m0, s51
	s_nop 0
	global_load_lds_dwordx4 v196, s[58:59] offset:0
	s_addc_u32 s37, s37, 0
	s_mov_b32 m0, s48
	s_nop 0
	global_load_lds_dwordx4 v197, s[36:37] offset:0
	s_nop 0
	s_mov_b32 m0, s49
	s_nop 0
	global_load_lds_dwordx4 v199, s[36:37] offset:0
	s_waitcnt vmcnt(8)
	s_waitcnt lgkmcnt(0)
	s_barrier
	s_setprio 1
	s_waitcnt lgkmcnt(7)
	v_mfma_f32_16x16x32_bf16 v[62:65], v[130:133], v[162:165], v[62:65]
	v_mfma_f32_16x16x32_bf16 v[58:61], v[134:137], v[162:165], v[58:61]
	s_waitcnt lgkmcnt(6)
	v_mfma_f32_16x16x32_bf16 v[54:57], v[130:133], v[166:169], v[54:57]
	v_mfma_f32_16x16x32_bf16 v[50:53], v[134:137], v[166:169], v[50:53]
	s_waitcnt lgkmcnt(3)
	v_mfma_f32_16x16x32_bf16 v[46:49], v[130:133], v[210:213], v[46:49]
	v_mfma_f32_16x16x32_bf16 v[42:45], v[134:137], v[210:213], v[42:45]
	s_waitcnt lgkmcnt(2)
	v_mfma_f32_16x16x32_bf16 v[38:41], v[130:133], v[214:217], v[38:41]
	v_mfma_f32_16x16x32_bf16 v[34:37], v[134:137], v[214:217], v[34:37]
	v_mfma_f32_16x16x32_bf16 v[62:65], v[138:141], v[178:181], v[62:65]
	v_mfma_f32_16x16x32_bf16 v[58:61], v[142:145], v[178:181], v[58:61]
	v_mfma_f32_16x16x32_bf16 v[54:57], v[138:141], v[182:185], v[54:57]
	v_mfma_f32_16x16x32_bf16 v[50:53], v[142:145], v[182:185], v[50:53]
	s_waitcnt lgkmcnt(1)
	v_mfma_f32_16x16x32_bf16 v[46:49], v[138:141], v[218:221], v[46:49]
	v_mfma_f32_16x16x32_bf16 v[42:45], v[142:145], v[218:221], v[42:45]
	s_waitcnt lgkmcnt(0)
	v_mfma_f32_16x16x32_bf16 v[38:41], v[138:141], v[222:225], v[38:41]
	v_mfma_f32_16x16x32_bf16 v[34:37], v[142:145], v[222:225], v[34:37]
	s_setprio 0
	s_setprio 1
	v_mfma_f32_16x16x32_bf16 v[30:33], v[146:149], v[162:165], v[30:33]
	v_mfma_f32_16x16x32_bf16 v[26:29], v[150:153], v[162:165], v[26:29]
	v_mfma_f32_16x16x32_bf16 v[22:25], v[146:149], v[166:169], v[22:25]
	v_mfma_f32_16x16x32_bf16 v[18:21], v[150:153], v[166:169], v[18:21]
	v_mfma_f32_16x16x32_bf16 v[14:17], v[146:149], v[210:213], v[14:17]
	v_mfma_f32_16x16x32_bf16 v[10:13], v[150:153], v[210:213], v[10:13]
	v_mfma_f32_16x16x32_bf16 v[6:9], v[146:149], v[214:217], v[6:9]
	v_mfma_f32_16x16x32_bf16 v[2:5], v[150:153], v[214:217], v[2:5]
	v_mfma_f32_16x16x32_bf16 v[30:33], v[154:157], v[178:181], v[30:33]
	v_mfma_f32_16x16x32_bf16 v[26:29], v[158:161], v[178:181], v[26:29]
	v_mfma_f32_16x16x32_bf16 v[22:25], v[154:157], v[182:185], v[22:25]
	v_mfma_f32_16x16x32_bf16 v[18:21], v[158:161], v[182:185], v[18:21]
	v_mfma_f32_16x16x32_bf16 v[14:17], v[154:157], v[218:221], v[14:17]
	v_mfma_f32_16x16x32_bf16 v[10:13], v[158:161], v[218:221], v[10:13]
	v_mfma_f32_16x16x32_bf16 v[6:9], v[154:157], v[222:225], v[6:9]
	v_mfma_f32_16x16x32_bf16 v[2:5], v[158:161], v[222:225], v[2:5]
	s_setprio 0
	s_add_i32 s31, s31, 2
	s_add_u32 s6, s6, 0x100
	s_addc_u32 s7, s7, 0
	s_barrier
.LBB0_368:
	.p2align 6
	s_nop 0
	ds_read_b128 v[130:133], v203
	ds_read_b128 v[134:137], v203 offset:2048
	ds_read_b128 v[138:141], v204
	ds_read_b128 v[142:145], v204 offset:2048
	ds_read_b128 v[146:149], v205
	ds_read_b128 v[150:153], v205 offset:2048
	ds_read_b128 v[154:157], v206
	ds_read_b128 v[158:161], v206 offset:2048
	ds_read_b128 v[162:165], v207
	ds_read_b128 v[166:169], v207 offset:2048
	ds_read_b128 v[174:177], v208
	ds_read_b128 v[178:181], v208 offset:2048
	ds_read_b128 v[182:185], v207 offset:4096
	ds_read_b128 v[210:213], v207 offset:6144
	ds_read_b128 v[214:217], v208 offset:4096
	ds_read_b128 v[218:221], v208 offset:6144
	s_add_u32 s36, s8, s6
	s_addc_u32 s37, s9, s7
	s_add_u32 s58, s36, 0x80
	s_addc_u32 s59, s37, 0
	s_mov_b32 m0, s52
	s_nop 0
	global_load_lds_dwordx4 v198, s[58:59] offset:0
	s_nop 0
	s_mov_b32 m0, s53
	s_nop 0
	global_load_lds_dwordx4 v200, s[58:59] offset:0
	s_waitcnt vmcnt(8)
	s_waitcnt lgkmcnt(0)
	s_barrier
	s_setprio 1
	s_waitcnt lgkmcnt(7)
	v_mfma_f32_16x16x32_bf16 v[126:129], v[130:133], v[162:165], v[126:129]
	v_mfma_f32_16x16x32_bf16 v[122:125], v[134:137], v[162:165], v[122:125]
	s_waitcnt lgkmcnt(6)
	v_mfma_f32_16x16x32_bf16 v[118:121], v[130:133], v[166:169], v[118:121]
	v_mfma_f32_16x16x32_bf16 v[114:117], v[134:137], v[166:169], v[114:117]
	s_waitcnt lgkmcnt(3)
	v_mfma_f32_16x16x32_bf16 v[110:113], v[130:133], v[182:185], v[110:113]
	v_mfma_f32_16x16x32_bf16 v[106:109], v[134:137], v[182:185], v[106:109]
	s_waitcnt lgkmcnt(2)
	v_mfma_f32_16x16x32_bf16 v[102:105], v[130:133], v[210:213], v[102:105]
	v_mfma_f32_16x16x32_bf16 v[98:101], v[134:137], v[210:213], v[98:101]
	v_mfma_f32_16x16x32_bf16 v[126:129], v[138:141], v[174:177], v[126:129]
	v_mfma_f32_16x16x32_bf16 v[122:125], v[142:145], v[174:177], v[122:125]
	v_mfma_f32_16x16x32_bf16 v[118:121], v[138:141], v[178:181], v[118:121]
	v_mfma_f32_16x16x32_bf16 v[114:117], v[142:145], v[178:181], v[114:117]
	s_waitcnt lgkmcnt(1)
	v_mfma_f32_16x16x32_bf16 v[110:113], v[138:141], v[214:217], v[110:113]
	v_mfma_f32_16x16x32_bf16 v[106:109], v[142:145], v[214:217], v[106:109]
	s_waitcnt lgkmcnt(0)
	v_mfma_f32_16x16x32_bf16 v[102:105], v[138:141], v[218:221], v[102:105]
	v_mfma_f32_16x16x32_bf16 v[98:101], v[142:145], v[218:221], v[98:101]
	s_setprio 0
	s_setprio 1
	v_mfma_f32_16x16x32_bf16 v[94:97], v[146:149], v[162:165], v[94:97]
	v_mfma_f32_16x16x32_bf16 v[90:93], v[150:153], v[162:165], v[90:93]
	v_mfma_f32_16x16x32_bf16 v[86:89], v[146:149], v[166:169], v[86:89]
	v_mfma_f32_16x16x32_bf16 v[82:85], v[150:153], v[166:169], v[82:85]
	v_mfma_f32_16x16x32_bf16 v[78:81], v[146:149], v[182:185], v[78:81]
	v_mfma_f32_16x16x32_bf16 v[74:77], v[150:153], v[182:185], v[74:77]
	v_mfma_f32_16x16x32_bf16 v[70:73], v[146:149], v[210:213], v[70:73]
	v_mfma_f32_16x16x32_bf16 v[66:69], v[150:153], v[210:213], v[66:69]
	v_mfma_f32_16x16x32_bf16 v[94:97], v[154:157], v[174:177], v[94:97]
	v_mfma_f32_16x16x32_bf16 v[90:93], v[158:161], v[174:177], v[90:93]
	v_mfma_f32_16x16x32_bf16 v[86:89], v[154:157], v[178:181], v[86:89]
	v_mfma_f32_16x16x32_bf16 v[82:85], v[158:161], v[178:181], v[82:85]
	v_mfma_f32_16x16x32_bf16 v[78:81], v[154:157], v[214:217], v[78:81]
	v_mfma_f32_16x16x32_bf16 v[74:77], v[158:161], v[214:217], v[74:77]
	v_mfma_f32_16x16x32_bf16 v[70:73], v[154:157], v[218:221], v[70:73]
	v_mfma_f32_16x16x32_bf16 v[66:69], v[158:161], v[218:221], v[66:69]
	s_setprio 0
	s_barrier
	s_add_u32 s60, s34, s6
	s_addc_u32 s61, s35, s7
	ds_read_b128 v[162:165], v207 offset:16384
	ds_read_b128 v[166:169], v207 offset:18432
	ds_read_b128 v[174:177], v208 offset:16384
	ds_read_b128 v[178:181], v208 offset:18432
	ds_read_b128 v[182:185], v207 offset:20480
	ds_read_b128 v[210:213], v207 offset:22528
	ds_read_b128 v[214:217], v208 offset:20480
	ds_read_b128 v[218:221], v208 offset:22528
	s_add_u32 s58, s60, 0x100
	s_addc_u32 s59, s61, 0
	s_mov_b32 m0, s39
	s_nop 0
	global_load_lds_dwordx4 v195, s[58:59] offset:0
	s_nop 0
	s_mov_b32 m0, s40
	s_nop 0
	global_load_lds_dwordx4 v196, s[58:59] offset:0
	s_add_u32 s58, s60, 0x40100
	s_addc_u32 s59, s61, 0
	s_mov_b32 m0, s41
	s_nop 0
	global_load_lds_dwordx4 v195, s[58:59] offset:0
	s_nop 0
	s_mov_b32 m0, s42
	s_nop 0
	global_load_lds_dwordx4 v196, s[58:59] offset:0
	s_add_u32 s58, s36, 0x100
	s_addc_u32 s59, s37, 0
	s_mov_b32 m0, s38
	s_nop 0
	global_load_lds_dwordx4 v197, s[58:59] offset:0
	s_nop 0
	s_mov_b32 m0, s43
	s_nop 0
	global_load_lds_dwordx4 v199, s[58:59] offset:0
	s_waitcnt vmcnt(8)
	s_waitcnt lgkmcnt(0)
	s_barrier
	s_setprio 1
	s_waitcnt lgkmcnt(7)
	v_mfma_f32_16x16x32_bf16 v[62:65], v[130:133], v[162:165], v[62:65]
	v_mfma_f32_16x16x32_bf16 v[58:61], v[134:137], v[162:165], v[58:61]
	s_waitcnt lgkmcnt(6)
	v_mfma_f32_16x16x32_bf16 v[54:57], v[130:133], v[166:169], v[54:57]
	v_mfma_f32_16x16x32_bf16 v[50:53], v[134:137], v[166:169], v[50:53]
	s_waitcnt lgkmcnt(3)
	v_mfma_f32_16x16x32_bf16 v[46:49], v[130:133], v[182:185], v[46:49]
	v_mfma_f32_16x16x32_bf16 v[42:45], v[134:137], v[182:185], v[42:45]
	s_waitcnt lgkmcnt(2)
	v_mfma_f32_16x16x32_bf16 v[38:41], v[130:133], v[210:213], v[38:41]
	v_mfma_f32_16x16x32_bf16 v[34:37], v[134:137], v[210:213], v[34:37]
	v_mfma_f32_16x16x32_bf16 v[62:65], v[138:141], v[174:177], v[62:65]
	v_mfma_f32_16x16x32_bf16 v[58:61], v[142:145], v[174:177], v[58:61]
	v_mfma_f32_16x16x32_bf16 v[54:57], v[138:141], v[178:181], v[54:57]
	v_mfma_f32_16x16x32_bf16 v[50:53], v[142:145], v[178:181], v[50:53]
	s_waitcnt lgkmcnt(1)
	v_mfma_f32_16x16x32_bf16 v[46:49], v[138:141], v[214:217], v[46:49]
	v_mfma_f32_16x16x32_bf16 v[42:45], v[142:145], v[214:217], v[42:45]
	s_waitcnt lgkmcnt(0)
	v_mfma_f32_16x16x32_bf16 v[38:41], v[138:141], v[218:221], v[38:41]
	v_mfma_f32_16x16x32_bf16 v[34:37], v[142:145], v[218:221], v[34:37]
	s_setprio 0
	s_setprio 1
	v_mfma_f32_16x16x32_bf16 v[30:33], v[146:149], v[162:165], v[30:33]
	v_mfma_f32_16x16x32_bf16 v[26:29], v[150:153], v[162:165], v[26:29]
	v_mfma_f32_16x16x32_bf16 v[22:25], v[146:149], v[166:169], v[22:25]
	v_mfma_f32_16x16x32_bf16 v[18:21], v[150:153], v[166:169], v[18:21]
	v_mfma_f32_16x16x32_bf16 v[14:17], v[146:149], v[182:185], v[14:17]
	v_mfma_f32_16x16x32_bf16 v[10:13], v[150:153], v[182:185], v[10:13]
	v_mfma_f32_16x16x32_bf16 v[6:9], v[146:149], v[210:213], v[6:9]
	v_mfma_f32_16x16x32_bf16 v[2:5], v[150:153], v[210:213], v[2:5]
	v_mfma_f32_16x16x32_bf16 v[30:33], v[154:157], v[174:177], v[30:33]
	v_mfma_f32_16x16x32_bf16 v[26:29], v[158:161], v[174:177], v[26:29]
	v_mfma_f32_16x16x32_bf16 v[22:25], v[154:157], v[178:181], v[22:25]
	v_mfma_f32_16x16x32_bf16 v[18:21], v[158:161], v[178:181], v[18:21]
	v_mfma_f32_16x16x32_bf16 v[14:17], v[154:157], v[214:217], v[14:17]
	v_mfma_f32_16x16x32_bf16 v[10:13], v[158:161], v[214:217], v[10:13]
	v_mfma_f32_16x16x32_bf16 v[6:9], v[154:157], v[218:221], v[6:9]
	v_mfma_f32_16x16x32_bf16 v[2:5], v[158:161], v[218:221], v[2:5]
	s_setprio 0
	s_barrier
	s_add_i32 s62, 0, 0x18000
	v_add_u32_e32 v174, s62, v201
	v_add_u32_e32 v175, s62, v202
	s_add_i32 s62, 0, 0x1c000
	v_add_u32_e32 v176, s62, v201
	ds_read_b128 v[130:133], v174
	ds_read_b128 v[134:137], v174 offset:2048
	ds_read_b128 v[138:141], v175
	ds_read_b128 v[142:145], v175 offset:2048
	v_add_u32_e32 v177, s62, v202
	ds_read_b128 v[146:149], v176
	ds_read_b128 v[150:153], v176 offset:2048
	ds_read_b128 v[154:157], v177
	ds_read_b128 v[158:161], v177 offset:2048
	ds_read_b128 v[162:165], v207 offset:32768
	ds_read_b128 v[166:169], v207 offset:34816
	ds_read_b128 v[178:181], v208 offset:32768
	ds_read_b128 v[182:185], v208 offset:34816
	ds_read_b128 v[210:213], v207 offset:36864
	ds_read_b128 v[214:217], v207 offset:38912
	ds_read_b128 v[218:221], v208 offset:36864
	ds_read_b128 v[222:225], v208 offset:38912
	s_mov_b32 m0, s44
	s_nop 0
	global_load_lds_dwordx4 v198, s[58:59] offset:0
	s_nop 0
	s_mov_b32 m0, s45
	s_nop 0
	global_load_lds_dwordx4 v200, s[58:59] offset:0
	s_waitcnt vmcnt(8)
	s_waitcnt lgkmcnt(0)
	s_barrier
	s_setprio 1
	s_waitcnt lgkmcnt(7)
	v_mfma_f32_16x16x32_bf16 v[126:129], v[130:133], v[162:165], v[126:129]
	v_mfma_f32_16x16x32_bf16 v[122:125], v[134:137], v[162:165], v[122:125]
	s_waitcnt lgkmcnt(6)
	v_mfma_f32_16x16x32_bf16 v[118:121], v[130:133], v[166:169], v[118:121]
	v_mfma_f32_16x16x32_bf16 v[114:117], v[134:137], v[166:169], v[114:117]
	s_waitcnt lgkmcnt(3)
	v_mfma_f32_16x16x32_bf16 v[110:113], v[130:133], v[210:213], v[110:113]
	v_mfma_f32_16x16x32_bf16 v[106:109], v[134:137], v[210:213], v[106:109]
	s_waitcnt lgkmcnt(2)
	v_mfma_f32_16x16x32_bf16 v[102:105], v[130:133], v[214:217], v[102:105]
	v_mfma_f32_16x16x32_bf16 v[98:101], v[134:137], v[214:217], v[98:101]
	v_mfma_f32_16x16x32_bf16 v[126:129], v[138:141], v[178:181], v[126:129]
	v_mfma_f32_16x16x32_bf16 v[122:125], v[142:145], v[178:181], v[122:125]
	v_mfma_f32_16x16x32_bf16 v[118:121], v[138:141], v[182:185], v[118:121]
	v_mfma_f32_16x16x32_bf16 v[114:117], v[142:145], v[182:185], v[114:117]
	s_waitcnt lgkmcnt(1)
	v_mfma_f32_16x16x32_bf16 v[110:113], v[138:141], v[218:221], v[110:113]
	v_mfma_f32_16x16x32_bf16 v[106:109], v[142:145], v[218:221], v[106:109]
	s_waitcnt lgkmcnt(0)
	v_mfma_f32_16x16x32_bf16 v[102:105], v[138:141], v[222:225], v[102:105]
	v_mfma_f32_16x16x32_bf16 v[98:101], v[142:145], v[222:225], v[98:101]
	s_setprio 0
	s_setprio 1
	v_mfma_f32_16x16x32_bf16 v[94:97], v[146:149], v[162:165], v[94:97]
	v_mfma_f32_16x16x32_bf16 v[90:93], v[150:153], v[162:165], v[90:93]
	v_mfma_f32_16x16x32_bf16 v[86:89], v[146:149], v[166:169], v[86:89]
	v_mfma_f32_16x16x32_bf16 v[82:85], v[150:153], v[166:169], v[82:85]
	v_mfma_f32_16x16x32_bf16 v[78:81], v[146:149], v[210:213], v[78:81]
	v_mfma_f32_16x16x32_bf16 v[74:77], v[150:153], v[210:213], v[74:77]
	v_mfma_f32_16x16x32_bf16 v[70:73], v[146:149], v[214:217], v[70:73]
	v_mfma_f32_16x16x32_bf16 v[66:69], v[150:153], v[214:217], v[66:69]
	v_mfma_f32_16x16x32_bf16 v[94:97], v[154:157], v[178:181], v[94:97]
	v_mfma_f32_16x16x32_bf16 v[90:93], v[158:161], v[178:181], v[90:93]
	v_mfma_f32_16x16x32_bf16 v[86:89], v[154:157], v[182:185], v[86:89]
	v_mfma_f32_16x16x32_bf16 v[82:85], v[158:161], v[182:185], v[82:85]
	v_mfma_f32_16x16x32_bf16 v[78:81], v[154:157], v[218:221], v[78:81]
	v_mfma_f32_16x16x32_bf16 v[74:77], v[158:161], v[218:221], v[74:77]
	v_mfma_f32_16x16x32_bf16 v[70:73], v[154:157], v[222:225], v[70:73]
	v_mfma_f32_16x16x32_bf16 v[66:69], v[158:161], v[222:225], v[66:69]
	s_setprio 0
	s_barrier
	ds_read_b128 v[162:165], v207 offset:49152
	ds_read_b128 v[166:169], v207 offset:51200
	ds_read_b128 v[178:181], v208 offset:49152
	ds_read_b128 v[182:185], v208 offset:51200
	ds_read_b128 v[210:213], v207 offset:53248
	ds_read_b128 v[214:217], v207 offset:55296
	ds_read_b128 v[218:221], v208 offset:53248
	ds_read_b128 v[222:225], v208 offset:55296
	s_add_u32 s58, s60, 0x180
	s_addc_u32 s59, s61, 0
	s_mov_b32 m0, s46
	s_nop 0
	global_load_lds_dwordx4 v195, s[58:59] offset:0
	s_nop 0
	s_mov_b32 m0, s47
	s_nop 0
	global_load_lds_dwordx4 v196, s[58:59] offset:0
	s_add_u32 s58, s60, 0x40180
	s_addc_u32 s59, s61, 0
	s_mov_b32 m0, s50
	s_nop 0
	global_load_lds_dwordx4 v195, s[58:59] offset:0
	s_add_u32 s36, s36, 0x180
	s_mov_b32 m0, s51
	s_nop 0
	global_load_lds_dwordx4 v196, s[58:59] offset:0
	s_addc_u32 s37, s37, 0
	s_mov_b32 m0, s48
	s_nop 0
	global_load_lds_dwordx4 v197, s[36:37] offset:0
	s_nop 0
	s_mov_b32 m0, s49
	s_nop 0
	global_load_lds_dwordx4 v199, s[36:37] offset:0
	s_waitcnt vmcnt(8)
	s_waitcnt lgkmcnt(0)
	s_barrier
	s_setprio 1
	s_waitcnt lgkmcnt(7)
	v_mfma_f32_16x16x32_bf16 v[62:65], v[130:133], v[162:165], v[62:65]
	v_mfma_f32_16x16x32_bf16 v[58:61], v[134:137], v[162:165], v[58:61]
	s_waitcnt lgkmcnt(6)
	v_mfma_f32_16x16x32_bf16 v[54:57], v[130:133], v[166:169], v[54:57]
	v_mfma_f32_16x16x32_bf16 v[50:53], v[134:137], v[166:169], v[50:53]
	s_waitcnt lgkmcnt(3)
	v_mfma_f32_16x16x32_bf16 v[46:49], v[130:133], v[210:213], v[46:49]
	v_mfma_f32_16x16x32_bf16 v[42:45], v[134:137], v[210:213], v[42:45]
	s_waitcnt lgkmcnt(2)
	v_mfma_f32_16x16x32_bf16 v[38:41], v[130:133], v[214:217], v[38:41]
	v_mfma_f32_16x16x32_bf16 v[34:37], v[134:137], v[214:217], v[34:37]
	v_mfma_f32_16x16x32_bf16 v[62:65], v[138:141], v[178:181], v[62:65]
	v_mfma_f32_16x16x32_bf16 v[58:61], v[142:145], v[178:181], v[58:61]
	v_mfma_f32_16x16x32_bf16 v[54:57], v[138:141], v[182:185], v[54:57]
	v_mfma_f32_16x16x32_bf16 v[50:53], v[142:145], v[182:185], v[50:53]
	s_waitcnt lgkmcnt(1)
	v_mfma_f32_16x16x32_bf16 v[46:49], v[138:141], v[218:221], v[46:49]
	v_mfma_f32_16x16x32_bf16 v[42:45], v[142:145], v[218:221], v[42:45]
	s_waitcnt lgkmcnt(0)
	v_mfma_f32_16x16x32_bf16 v[38:41], v[138:141], v[222:225], v[38:41]
	v_mfma_f32_16x16x32_bf16 v[34:37], v[142:145], v[222:225], v[34:37]
	s_setprio 0
	s_setprio 1
	v_mfma_f32_16x16x32_bf16 v[30:33], v[146:149], v[162:165], v[30:33]
	v_mfma_f32_16x16x32_bf16 v[26:29], v[150:153], v[162:165], v[26:29]
	v_mfma_f32_16x16x32_bf16 v[22:25], v[146:149], v[166:169], v[22:25]
	v_mfma_f32_16x16x32_bf16 v[18:21], v[150:153], v[166:169], v[18:21]
	v_mfma_f32_16x16x32_bf16 v[14:17], v[146:149], v[210:213], v[14:17]
	v_mfma_f32_16x16x32_bf16 v[10:13], v[150:153], v[210:213], v[10:13]
	v_mfma_f32_16x16x32_bf16 v[6:9], v[146:149], v[214:217], v[6:9]
	v_mfma_f32_16x16x32_bf16 v[2:5], v[150:153], v[214:217], v[2:5]
	v_mfma_f32_16x16x32_bf16 v[30:33], v[154:157], v[178:181], v[30:33]
	v_mfma_f32_16x16x32_bf16 v[26:29], v[158:161], v[178:181], v[26:29]
	v_mfma_f32_16x16x32_bf16 v[22:25], v[154:157], v[182:185], v[22:25]
	v_mfma_f32_16x16x32_bf16 v[18:21], v[158:161], v[182:185], v[18:21]
	v_mfma_f32_16x16x32_bf16 v[14:17], v[154:157], v[218:221], v[14:17]
	v_mfma_f32_16x16x32_bf16 v[10:13], v[158:161], v[218:221], v[10:13]
	v_mfma_f32_16x16x32_bf16 v[6:9], v[154:157], v[222:225], v[6:9]
	v_mfma_f32_16x16x32_bf16 v[2:5], v[158:161], v[222:225], v[2:5]
	s_setprio 0
	s_add_i32 s31, s31, 2
	s_add_u32 s6, s6, 0x100
	s_addc_u32 s7, s7, 0
	s_cmp_lt_u32 s31, 12
	s_barrier
	s_cbranch_scc1 .LBB0_368
	ds_read_b128 v[154:157], v203
	ds_read_b128 v[158:161], v203 offset:2048
	ds_read_b128 v[166:169], v204
	ds_read_b128 v[162:165], v204 offset:2048
	ds_read_b128 v[138:141], v205
	ds_read_b128 v[142:145], v205 offset:2048
	ds_read_b128 v[150:153], v206
	ds_read_b128 v[146:149], v206 offset:2048
	ds_read_b128 v[134:137], v207
	ds_read_b128 v[178:181], v207 offset:2048
	ds_read_b128 v[182:185], v208
	ds_read_b128 v[210:213], v208 offset:2048
	ds_read_b128 v[214:217], v207 offset:4096
	ds_read_b128 v[218:221], v207 offset:6144
	ds_read_b128 v[222:225], v208 offset:4096
	ds_read_b128 v[226:229], v208 offset:6144
	s_mov_b32 m0, s52
	s_nop 0
	global_load_lds_dwordx4 v198, s[20:21] offset:0
	s_nop 0
	s_mov_b32 m0, s53
	s_nop 0
	global_load_lds_dwordx4 v200, s[20:21] offset:0
	s_waitcnt vmcnt(8)
	s_waitcnt lgkmcnt(0)
	s_barrier
	s_setprio 1
	s_waitcnt lgkmcnt(7)
	v_mfma_f32_16x16x32_bf16 v[126:129], v[154:157], v[134:137], v[126:129]
	v_mfma_f32_16x16x32_bf16 v[122:125], v[158:161], v[134:137], v[122:125]
	s_waitcnt lgkmcnt(6)
	v_mfma_f32_16x16x32_bf16 v[118:121], v[154:157], v[178:181], v[118:121]
	v_mfma_f32_16x16x32_bf16 v[114:117], v[158:161], v[178:181], v[114:117]
	s_waitcnt lgkmcnt(3)
	v_mfma_f32_16x16x32_bf16 v[110:113], v[154:157], v[214:217], v[110:113]
	v_mfma_f32_16x16x32_bf16 v[106:109], v[158:161], v[214:217], v[106:109]
	s_waitcnt lgkmcnt(2)
	v_mfma_f32_16x16x32_bf16 v[102:105], v[154:157], v[218:221], v[102:105]
	v_mfma_f32_16x16x32_bf16 v[98:101], v[158:161], v[218:221], v[98:101]
	v_mfma_f32_16x16x32_bf16 v[126:129], v[166:169], v[182:185], v[126:129]
	v_mfma_f32_16x16x32_bf16 v[122:125], v[162:165], v[182:185], v[122:125]
	v_mfma_f32_16x16x32_bf16 v[118:121], v[166:169], v[210:213], v[118:121]
	v_mfma_f32_16x16x32_bf16 v[114:117], v[162:165], v[210:213], v[114:117]
	s_waitcnt lgkmcnt(1)
	v_mfma_f32_16x16x32_bf16 v[110:113], v[166:169], v[222:225], v[110:113]
	v_mfma_f32_16x16x32_bf16 v[106:109], v[162:165], v[222:225], v[106:109]
	s_waitcnt lgkmcnt(0)
	v_mfma_f32_16x16x32_bf16 v[102:105], v[166:169], v[226:229], v[102:105]
	v_mfma_f32_16x16x32_bf16 v[98:101], v[162:165], v[226:229], v[98:101]
	s_setprio 0
	s_setprio 1
	v_mfma_f32_16x16x32_bf16 v[94:97], v[138:141], v[134:137], v[94:97]
	v_mfma_f32_16x16x32_bf16 v[90:93], v[142:145], v[134:137], v[90:93]
	v_mfma_f32_16x16x32_bf16 v[86:89], v[138:141], v[178:181], v[86:89]
	v_mfma_f32_16x16x32_bf16 v[82:85], v[142:145], v[178:181], v[82:85]
	v_mfma_f32_16x16x32_bf16 v[78:81], v[138:141], v[214:217], v[78:81]
	v_mfma_f32_16x16x32_bf16 v[74:77], v[142:145], v[214:217], v[74:77]
	v_mfma_f32_16x16x32_bf16 v[70:73], v[138:141], v[218:221], v[70:73]
	v_mfma_f32_16x16x32_bf16 v[66:69], v[142:145], v[218:221], v[66:69]
	v_mfma_f32_16x16x32_bf16 v[130:133], v[150:153], v[182:185], v[94:97]
	v_mfma_f32_16x16x32_bf16 v[134:137], v[146:149], v[182:185], v[90:93]
	v_mfma_f32_16x16x32_bf16 v[86:89], v[150:153], v[210:213], v[86:89]
	v_mfma_f32_16x16x32_bf16 v[82:85], v[146:149], v[210:213], v[82:85]
	v_mfma_f32_16x16x32_bf16 v[78:81], v[150:153], v[222:225], v[78:81]
	v_mfma_f32_16x16x32_bf16 v[74:77], v[146:149], v[222:225], v[74:77]
	v_mfma_f32_16x16x32_bf16 v[70:73], v[150:153], v[226:229], v[70:73]
	v_mfma_f32_16x16x32_bf16 v[66:69], v[146:149], v[226:229], v[66:69]
	s_setprio 0
	s_barrier
	v_cndmask_b32_e64 v90, 0, 1, s[4:5]
	v_cmp_ne_u32_e64 s[6:7], 1, v90
	s_andn2_b64 vcc, exec, s[4:5]
	s_cbranch_vccnz .LBB0_371
	v_mov_b32_e32 v90, v0
	s_nop 0
	v_lshlrev_b32_e32 v91, 4, v90
	v_bitop3_b32 v91, v91, s3, v90 bitop3:0x48
	v_lshlrev_b32_e32 v90, 8, v90
	v_lshl_or_b32 v91, s55, 19, v91
	v_and_b32_e32 v90, 0xfffff800, v90
	v_add_u32_e32 v197, v91, v90
	v_add_u32_e32 v198, 0x40000, v197
	v_add_u32_e32 v199, 0x20000, v197
	v_add_u32_e32 v200, 0x60000, v197

.LBB0_560:
	s_mov_b32 s35, -2
	.p2align 6
	s_nop 0
	ds_read_b128 v[18:21], v179
	ds_read_b128 v[26:29], v179 offset:2048
	ds_read_b128 v[22:25], v180
	ds_read_b128 v[30:33], v180 offset:2048
	ds_read_b128 v[2:5], v181
	ds_read_b128 v[10:13], v181 offset:2048
	ds_read_b128 v[6:9], v182
	ds_read_b128 v[14:17], v182 offset:2048
	ds_read_b128 v[194:197], v183
	ds_read_b128 v[202:205], v183 offset:2048
	ds_read_b128 v[198:201], v184
	ds_read_b128 v[206:209], v184 offset:2048
	ds_read_b128 v[210:213], v183 offset:4096
	ds_read_b128 v[218:221], v183 offset:6144
	ds_read_b128 v[214:217], v184 offset:4096
	ds_read_b128 v[222:225], v184 offset:6144
	s_add_u32 s39, s18, s4
	s_addc_u32 s68, s19, s5
	s_add_u32 s42, s39, 0x80
	s_addc_u32 s43, s68, 0
	s_mov_b32 m0, s61
	s_nop 0
	global_load_lds_dwordx4 v172, s[42:43] offset:0
	s_nop 0
	s_mov_b32 m0, s62
	s_nop 0
	global_load_lds_dwordx4 v175, s[42:43] offset:0
	s_waitcnt vmcnt(8)
	s_waitcnt lgkmcnt(0)
	s_barrier
	s_setprio 1
	s_waitcnt lgkmcnt(5)
	v_mfma_f32_16x16x128_f8f6f4 v[158:161], v[18:25], v[194:201], 0
	v_mfma_f32_16x16x128_f8f6f4 v[150:153], v[26:33], v[194:201], 0
	s_waitcnt lgkmcnt(4)
	v_mfma_f32_16x16x128_f8f6f4 v[142:145], v[18:25], v[202:209], 0
	v_mfma_f32_16x16x128_f8f6f4 v[134:137], v[26:33], v[202:209], 0
	s_waitcnt lgkmcnt(1)
	v_mfma_f32_16x16x128_f8f6f4 v[126:129], v[18:25], v[210:217], 0
	v_mfma_f32_16x16x128_f8f6f4 v[118:121], v[26:33], v[210:217], 0
	s_waitcnt lgkmcnt(0)
	v_mfma_f32_16x16x128_f8f6f4 v[110:113], v[18:25], v[218:225], 0
	v_mfma_f32_16x16x128_f8f6f4 v[102:105], v[26:33], v[218:225], 0
	s_setprio 0
	s_setprio 1
	v_mfma_f32_16x16x128_f8f6f4 v[154:157], v[2:9], v[194:201], 0
	v_mfma_f32_16x16x128_f8f6f4 v[146:149], v[10:17], v[194:201], 0
	v_mfma_f32_16x16x128_f8f6f4 v[138:141], v[2:9], v[202:209], 0
	v_mfma_f32_16x16x128_f8f6f4 v[130:133], v[10:17], v[202:209], 0
	v_mfma_f32_16x16x128_f8f6f4 v[122:125], v[2:9], v[210:217], 0
	v_mfma_f32_16x16x128_f8f6f4 v[114:117], v[10:17], v[210:217], 0
	v_mfma_f32_16x16x128_f8f6f4 v[106:109], v[2:9], v[218:225], 0
	v_mfma_f32_16x16x128_f8f6f4 v[98:101], v[10:17], v[218:225], 0
	s_setprio 0
	s_barrier
	s_add_u32 s69, s44, s4
	s_addc_u32 s70, s45, s5
	ds_read_b128 v[194:197], v183 offset:16384
	ds_read_b128 v[202:205], v183 offset:18432
	ds_read_b128 v[198:201], v184 offset:16384
	ds_read_b128 v[206:209], v184 offset:18432
	ds_read_b128 v[210:213], v183 offset:20480
	ds_read_b128 v[218:221], v183 offset:22528
	ds_read_b128 v[214:217], v184 offset:20480
	ds_read_b128 v[222:225], v184 offset:22528
	s_add_u32 s42, s69, 0x100
	s_addc_u32 s43, s70, 0
	s_mov_b32 m0, s48
	s_nop 0
	global_load_lds_dwordx4 v1, s[42:43] offset:0
	s_nop 0
	s_mov_b32 m0, s49
	s_nop 0
	global_load_lds_dwordx4 v173, s[42:43] offset:0
	s_add_u32 s42, s69, 0x20100
	s_addc_u32 s43, s70, 0
	s_mov_b32 m0, s50
	s_nop 0
	global_load_lds_dwordx4 v1, s[42:43] offset:0
	s_nop 0
	s_mov_b32 m0, s51
	s_nop 0
	global_load_lds_dwordx4 v173, s[42:43] offset:0
	s_add_u32 s42, s39, 0x100
	s_addc_u32 s43, s68, 0
	s_mov_b32 m0, s29
	s_nop 0
	global_load_lds_dwordx4 v171, s[42:43] offset:0
	s_nop 0
	s_mov_b32 m0, s52
	s_nop 0
	global_load_lds_dwordx4 v174, s[42:43] offset:0
	s_waitcnt vmcnt(8)
	s_waitcnt lgkmcnt(0)
	s_barrier
	s_setprio 1
	s_waitcnt lgkmcnt(5)
	v_mfma_f32_16x16x128_f8f6f4 v[94:97], v[18:25], v[194:201], 0
	v_mfma_f32_16x16x128_f8f6f4 v[86:89], v[26:33], v[194:201], 0
	s_waitcnt lgkmcnt(4)
	v_mfma_f32_16x16x128_f8f6f4 v[78:81], v[18:25], v[202:209], 0
	v_mfma_f32_16x16x128_f8f6f4 v[70:73], v[26:33], v[202:209], 0
	s_waitcnt lgkmcnt(1)
	v_mfma_f32_16x16x128_f8f6f4 v[62:65], v[18:25], v[210:217], 0
	v_mfma_f32_16x16x128_f8f6f4 v[54:57], v[26:33], v[210:217], 0
	s_waitcnt lgkmcnt(0)
	v_mfma_f32_16x16x128_f8f6f4 v[46:49], v[18:25], v[218:225], 0
	v_mfma_f32_16x16x128_f8f6f4 v[38:41], v[26:33], v[218:225], 0
	s_setprio 0
	s_setprio 1
	v_mfma_f32_16x16x128_f8f6f4 v[90:93], v[2:9], v[194:201], 0
	v_mfma_f32_16x16x128_f8f6f4 v[82:85], v[10:17], v[194:201], 0
	v_mfma_f32_16x16x128_f8f6f4 v[74:77], v[2:9], v[202:209], 0
	v_mfma_f32_16x16x128_f8f6f4 v[66:69], v[10:17], v[202:209], 0
	v_mfma_f32_16x16x128_f8f6f4 v[58:61], v[2:9], v[210:217], 0
	v_mfma_f32_16x16x128_f8f6f4 v[50:53], v[10:17], v[210:217], 0
	v_mfma_f32_16x16x128_f8f6f4 v[42:45], v[2:9], v[218:225], 0
	v_mfma_f32_16x16x128_f8f6f4 v[34:37], v[10:17], v[218:225], 0
	s_setprio 0
	s_barrier
	s_add_i32 s71, 0, 0x18000
	v_add_u32_e32 v162, s71, v176
	v_add_u32_e32 v187, s71, v177
	s_add_i32 s71, 0, 0x1c000
	v_add_u32_e32 v194, s71, v176
	ds_read_b128 v[2:5], v162
	ds_read_b128 v[10:13], v162 offset:2048
	ds_read_b128 v[6:9], v187
	ds_read_b128 v[14:17], v187 offset:2048
	v_add_u32_e32 v195, s71, v177
	ds_read_b128 v[18:21], v194
	ds_read_b128 v[26:29], v194 offset:2048
	ds_read_b128 v[22:25], v195
	ds_read_b128 v[30:33], v195 offset:2048
	ds_read_b128 v[196:199], v183 offset:32768
	ds_read_b128 v[204:207], v183 offset:34816
	ds_read_b128 v[200:203], v184 offset:32768
	ds_read_b128 v[208:211], v184 offset:34816
	ds_read_b128 v[212:215], v183 offset:36864
	ds_read_b128 v[220:223], v183 offset:38912
	ds_read_b128 v[216:219], v184 offset:36864
	ds_read_b128 v[224:227], v184 offset:38912
	s_mov_b32 m0, s53
	s_nop 0
	global_load_lds_dwordx4 v172, s[42:43] offset:0
	s_nop 0
	s_mov_b32 m0, s54
	s_nop 0
	global_load_lds_dwordx4 v175, s[42:43] offset:0
	s_waitcnt vmcnt(8)
	s_waitcnt lgkmcnt(0)
	s_barrier
	s_setprio 1
	s_waitcnt lgkmcnt(5)
	v_mfma_f32_16x16x128_f8f6f4 v[158:161], v[2:9], v[196:203], v[158:161]
	v_mfma_f32_16x16x128_f8f6f4 v[150:153], v[10:17], v[196:203], v[150:153]
	s_waitcnt lgkmcnt(4)
	v_mfma_f32_16x16x128_f8f6f4 v[142:145], v[2:9], v[204:211], v[142:145]
	v_mfma_f32_16x16x128_f8f6f4 v[134:137], v[10:17], v[204:211], v[134:137]
	s_waitcnt lgkmcnt(1)
	v_mfma_f32_16x16x128_f8f6f4 v[126:129], v[2:9], v[212:219], v[126:129]
	v_mfma_f32_16x16x128_f8f6f4 v[118:121], v[10:17], v[212:219], v[118:121]
	s_waitcnt lgkmcnt(0)
	v_mfma_f32_16x16x128_f8f6f4 v[110:113], v[2:9], v[220:227], v[110:113]
	v_mfma_f32_16x16x128_f8f6f4 v[102:105], v[10:17], v[220:227], v[102:105]
	s_setprio 0
	s_setprio 1
	v_mfma_f32_16x16x128_f8f6f4 v[154:157], v[18:25], v[196:203], v[154:157]
	v_mfma_f32_16x16x128_f8f6f4 v[146:149], v[26:33], v[196:203], v[146:149]
	v_mfma_f32_16x16x128_f8f6f4 v[138:141], v[18:25], v[204:211], v[138:141]
	v_mfma_f32_16x16x128_f8f6f4 v[130:133], v[26:33], v[204:211], v[130:133]
	v_mfma_f32_16x16x128_f8f6f4 v[122:125], v[18:25], v[212:219], v[122:125]
	v_mfma_f32_16x16x128_f8f6f4 v[114:117], v[26:33], v[212:219], v[114:117]
	v_mfma_f32_16x16x128_f8f6f4 v[106:109], v[18:25], v[220:227], v[106:109]
	v_mfma_f32_16x16x128_f8f6f4 v[98:101], v[26:33], v[220:227], v[98:101]
	s_setprio 0
	s_barrier
	ds_read_b128 v[196:199], v183 offset:49152
	ds_read_b128 v[204:207], v183 offset:51200
	ds_read_b128 v[200:203], v184 offset:49152
	ds_read_b128 v[208:211], v184 offset:51200
	ds_read_b128 v[212:215], v183 offset:53248
	ds_read_b128 v[220:223], v183 offset:55296
	ds_read_b128 v[216:219], v184 offset:53248
	ds_read_b128 v[224:227], v184 offset:55296
	s_add_u32 s42, s69, 0x180
	s_addc_u32 s43, s70, 0
	s_mov_b32 m0, s55
	s_nop 0
	global_load_lds_dwordx4 v1, s[42:43] offset:0
	s_nop 0
	s_mov_b32 m0, s56
	s_nop 0
	global_load_lds_dwordx4 v173, s[42:43] offset:0
	s_add_u32 s42, s69, 0x20180
	s_addc_u32 s43, s70, 0
	s_mov_b32 m0, s59
	s_nop 0
	global_load_lds_dwordx4 v1, s[42:43] offset:0
	s_nop 0
	s_mov_b32 m0, s60
	s_nop 0
	global_load_lds_dwordx4 v173, s[42:43] offset:0
	s_add_u32 s42, s39, 0x180
	s_addc_u32 s43, s68, 0
	s_mov_b32 m0, s57
	s_nop 0
	global_load_lds_dwordx4 v171, s[42:43] offset:0
	s_nop 0
	s_mov_b32 m0, s58
	s_nop 0
	global_load_lds_dwordx4 v174, s[42:43] offset:0
	s_waitcnt vmcnt(8)
	s_waitcnt lgkmcnt(0)
	s_barrier
	s_setprio 1
	s_waitcnt lgkmcnt(5)
	v_mfma_f32_16x16x128_f8f6f4 v[94:97], v[2:9], v[196:203], v[94:97]
	v_mfma_f32_16x16x128_f8f6f4 v[86:89], v[10:17], v[196:203], v[86:89]
	s_waitcnt lgkmcnt(4)
	v_mfma_f32_16x16x128_f8f6f4 v[78:81], v[2:9], v[204:211], v[78:81]
	v_mfma_f32_16x16x128_f8f6f4 v[70:73], v[10:17], v[204:211], v[70:73]
	s_waitcnt lgkmcnt(1)
	v_mfma_f32_16x16x128_f8f6f4 v[62:65], v[2:9], v[212:219], v[62:65]
	v_mfma_f32_16x16x128_f8f6f4 v[54:57], v[10:17], v[212:219], v[54:57]
	s_waitcnt lgkmcnt(0)
	v_mfma_f32_16x16x128_f8f6f4 v[46:49], v[2:9], v[220:227], v[46:49]
	v_mfma_f32_16x16x128_f8f6f4 v[38:41], v[10:17], v[220:227], v[38:41]
	s_setprio 0
	s_setprio 1
	v_mfma_f32_16x16x128_f8f6f4 v[90:93], v[18:25], v[196:203], v[90:93]
	v_mfma_f32_16x16x128_f8f6f4 v[82:85], v[26:33], v[196:203], v[82:85]
	v_mfma_f32_16x16x128_f8f6f4 v[74:77], v[18:25], v[204:211], v[74:77]
	v_mfma_f32_16x16x128_f8f6f4 v[66:69], v[26:33], v[204:211], v[66:69]
	v_mfma_f32_16x16x128_f8f6f4 v[58:61], v[18:25], v[212:219], v[58:61]
	v_mfma_f32_16x16x128_f8f6f4 v[50:53], v[26:33], v[212:219], v[50:53]
	v_mfma_f32_16x16x128_f8f6f4 v[42:45], v[18:25], v[220:227], v[42:45]
	v_mfma_f32_16x16x128_f8f6f4 v[34:37], v[26:33], v[220:227], v[34:37]
	s_setprio 0
	s_add_i32 s35, s35, 2
	s_add_u32 s4, s4, 0x100
	s_addc_u32 s5, s5, 0
	s_barrier
.LBB0_561:
	.p2align 6
	s_nop 0
	ds_read_b128 v[18:21], v179
	ds_read_b128 v[26:29], v179 offset:2048
	ds_read_b128 v[22:25], v180
	ds_read_b128 v[30:33], v180 offset:2048
	ds_read_b128 v[2:5], v181
	ds_read_b128 v[10:13], v181 offset:2048
	ds_read_b128 v[6:9], v182
	ds_read_b128 v[14:17], v182 offset:2048
	ds_read_b128 v[194:197], v183
	ds_read_b128 v[202:205], v183 offset:2048
	ds_read_b128 v[198:201], v184
	ds_read_b128 v[206:209], v184 offset:2048
	ds_read_b128 v[210:213], v183 offset:4096
	ds_read_b128 v[218:221], v183 offset:6144
	ds_read_b128 v[214:217], v184 offset:4096
	ds_read_b128 v[222:225], v184 offset:6144
	s_add_u32 s39, s18, s4
	s_addc_u32 s68, s19, s5
	s_add_u32 s42, s39, 0x80
	s_addc_u32 s43, s68, 0
	s_mov_b32 m0, s61
	s_nop 0
	global_load_lds_dwordx4 v172, s[42:43] offset:0
	s_nop 0
	s_mov_b32 m0, s62
	s_nop 0
	global_load_lds_dwordx4 v175, s[42:43] offset:0
	s_waitcnt vmcnt(8)
	s_waitcnt lgkmcnt(0)
	s_barrier
	s_setprio 1
	s_waitcnt lgkmcnt(5)
	v_mfma_f32_16x16x128_f8f6f4 v[158:161], v[18:25], v[194:201], v[158:161]
	v_mfma_f32_16x16x128_f8f6f4 v[150:153], v[26:33], v[194:201], v[150:153]
	s_waitcnt lgkmcnt(4)
	v_mfma_f32_16x16x128_f8f6f4 v[142:145], v[18:25], v[202:209], v[142:145]
	v_mfma_f32_16x16x128_f8f6f4 v[134:137], v[26:33], v[202:209], v[134:137]
	s_waitcnt lgkmcnt(1)
	v_mfma_f32_16x16x128_f8f6f4 v[126:129], v[18:25], v[210:217], v[126:129]
	v_mfma_f32_16x16x128_f8f6f4 v[118:121], v[26:33], v[210:217], v[118:121]
	s_waitcnt lgkmcnt(0)
	v_mfma_f32_16x16x128_f8f6f4 v[110:113], v[18:25], v[218:225], v[110:113]
	v_mfma_f32_16x16x128_f8f6f4 v[102:105], v[26:33], v[218:225], v[102:105]
	s_setprio 0
	s_setprio 1
	v_mfma_f32_16x16x128_f8f6f4 v[154:157], v[2:9], v[194:201], v[154:157]
	v_mfma_f32_16x16x128_f8f6f4 v[146:149], v[10:17], v[194:201], v[146:149]
	v_mfma_f32_16x16x128_f8f6f4 v[138:141], v[2:9], v[202:209], v[138:141]
	v_mfma_f32_16x16x128_f8f6f4 v[130:133], v[10:17], v[202:209], v[130:133]
	v_mfma_f32_16x16x128_f8f6f4 v[122:125], v[2:9], v[210:217], v[122:125]
	v_mfma_f32_16x16x128_f8f6f4 v[114:117], v[10:17], v[210:217], v[114:117]
	v_mfma_f32_16x16x128_f8f6f4 v[106:109], v[2:9], v[218:225], v[106:109]
	v_mfma_f32_16x16x128_f8f6f4 v[98:101], v[10:17], v[218:225], v[98:101]
	s_setprio 0
	s_barrier
	s_add_u32 s69, s44, s4
	s_addc_u32 s70, s45, s5
	ds_read_b128 v[194:197], v183 offset:16384
	ds_read_b128 v[202:205], v183 offset:18432
	ds_read_b128 v[198:201], v184 offset:16384
	ds_read_b128 v[206:209], v184 offset:18432
	ds_read_b128 v[210:213], v183 offset:20480
	ds_read_b128 v[218:221], v183 offset:22528
	ds_read_b128 v[214:217], v184 offset:20480
	ds_read_b128 v[222:225], v184 offset:22528
	s_add_u32 s42, s69, 0x100
	s_addc_u32 s43, s70, 0
	s_mov_b32 m0, s48
	s_nop 0
	global_load_lds_dwordx4 v1, s[42:43] offset:0
	s_nop 0
	s_mov_b32 m0, s49
	s_nop 0
	global_load_lds_dwordx4 v173, s[42:43] offset:0
	s_add_u32 s42, s69, 0x20100
	s_addc_u32 s43, s70, 0
	s_mov_b32 m0, s50
	s_nop 0
	global_load_lds_dwordx4 v1, s[42:43] offset:0
	s_nop 0
	s_mov_b32 m0, s51
	s_nop 0
	global_load_lds_dwordx4 v173, s[42:43] offset:0
	s_add_u32 s42, s39, 0x100
	s_addc_u32 s43, s68, 0
	s_mov_b32 m0, s29
	s_nop 0
	global_load_lds_dwordx4 v171, s[42:43] offset:0
	s_nop 0
	s_mov_b32 m0, s52
	s_nop 0
	global_load_lds_dwordx4 v174, s[42:43] offset:0
	s_waitcnt vmcnt(8)
	s_waitcnt lgkmcnt(0)
	s_barrier
	s_setprio 1
	s_waitcnt lgkmcnt(5)
	v_mfma_f32_16x16x128_f8f6f4 v[94:97], v[18:25], v[194:201], v[94:97]
	v_mfma_f32_16x16x128_f8f6f4 v[86:89], v[26:33], v[194:201], v[86:89]
	s_waitcnt lgkmcnt(4)
	v_mfma_f32_16x16x128_f8f6f4 v[78:81], v[18:25], v[202:209], v[78:81]
	v_mfma_f32_16x16x128_f8f6f4 v[70:73], v[26:33], v[202:209], v[70:73]
	s_waitcnt lgkmcnt(1)
	v_mfma_f32_16x16x128_f8f6f4 v[62:65], v[18:25], v[210:217], v[62:65]
	v_mfma_f32_16x16x128_f8f6f4 v[54:57], v[26:33], v[210:217], v[54:57]
	s_waitcnt lgkmcnt(0)
	v_mfma_f32_16x16x128_f8f6f4 v[46:49], v[18:25], v[218:225], v[46:49]
	v_mfma_f32_16x16x128_f8f6f4 v[38:41], v[26:33], v[218:225], v[38:41]
	s_setprio 0
	s_setprio 1
	v_mfma_f32_16x16x128_f8f6f4 v[90:93], v[2:9], v[194:201], v[90:93]
	v_mfma_f32_16x16x128_f8f6f4 v[82:85], v[10:17], v[194:201], v[82:85]
	v_mfma_f32_16x16x128_f8f6f4 v[74:77], v[2:9], v[202:209], v[74:77]
	v_mfma_f32_16x16x128_f8f6f4 v[66:69], v[10:17], v[202:209], v[66:69]
	v_mfma_f32_16x16x128_f8f6f4 v[58:61], v[2:9], v[210:217], v[58:61]
	v_mfma_f32_16x16x128_f8f6f4 v[50:53], v[10:17], v[210:217], v[50:53]
	v_mfma_f32_16x16x128_f8f6f4 v[42:45], v[2:9], v[218:225], v[42:45]
	v_mfma_f32_16x16x128_f8f6f4 v[34:37], v[10:17], v[218:225], v[34:37]
	s_setprio 0
	s_barrier
	s_add_i32 s71, 0, 0x18000
	v_add_u32_e32 v162, s71, v176
	v_add_u32_e32 v187, s71, v177
	s_add_i32 s71, 0, 0x1c000
	v_add_u32_e32 v194, s71, v176
	ds_read_b128 v[2:5], v162
	ds_read_b128 v[10:13], v162 offset:2048
	ds_read_b128 v[6:9], v187
	ds_read_b128 v[14:17], v187 offset:2048
	v_add_u32_e32 v195, s71, v177
	ds_read_b128 v[18:21], v194
	ds_read_b128 v[26:29], v194 offset:2048
	ds_read_b128 v[22:25], v195
	ds_read_b128 v[30:33], v195 offset:2048
	ds_read_b128 v[196:199], v183 offset:32768
	ds_read_b128 v[204:207], v183 offset:34816
	ds_read_b128 v[200:203], v184 offset:32768
	ds_read_b128 v[208:211], v184 offset:34816
	ds_read_b128 v[212:215], v183 offset:36864
	ds_read_b128 v[220:223], v183 offset:38912
	ds_read_b128 v[216:219], v184 offset:36864
	ds_read_b128 v[224:227], v184 offset:38912
	s_mov_b32 m0, s53
	s_nop 0
	global_load_lds_dwordx4 v172, s[42:43] offset:0
	s_nop 0
	s_mov_b32 m0, s54
	s_nop 0
	global_load_lds_dwordx4 v175, s[42:43] offset:0
	s_waitcnt vmcnt(8)
	s_waitcnt lgkmcnt(0)
	s_barrier
	s_setprio 1
	s_waitcnt lgkmcnt(5)
	v_mfma_f32_16x16x128_f8f6f4 v[158:161], v[2:9], v[196:203], v[158:161]
	v_mfma_f32_16x16x128_f8f6f4 v[150:153], v[10:17], v[196:203], v[150:153]
	s_waitcnt lgkmcnt(4)
	v_mfma_f32_16x16x128_f8f6f4 v[142:145], v[2:9], v[204:211], v[142:145]
	v_mfma_f32_16x16x128_f8f6f4 v[134:137], v[10:17], v[204:211], v[134:137]
	s_waitcnt lgkmcnt(1)
	v_mfma_f32_16x16x128_f8f6f4 v[126:129], v[2:9], v[212:219], v[126:129]
	v_mfma_f32_16x16x128_f8f6f4 v[118:121], v[10:17], v[212:219], v[118:121]
	s_waitcnt lgkmcnt(0)
	v_mfma_f32_16x16x128_f8f6f4 v[110:113], v[2:9], v[220:227], v[110:113]
	v_mfma_f32_16x16x128_f8f6f4 v[102:105], v[10:17], v[220:227], v[102:105]
	s_setprio 0
	s_setprio 1
	v_mfma_f32_16x16x128_f8f6f4 v[154:157], v[18:25], v[196:203], v[154:157]
	v_mfma_f32_16x16x128_f8f6f4 v[146:149], v[26:33], v[196:203], v[146:149]
	v_mfma_f32_16x16x128_f8f6f4 v[138:141], v[18:25], v[204:211], v[138:141]
	v_mfma_f32_16x16x128_f8f6f4 v[130:133], v[26:33], v[204:211], v[130:133]
	v_mfma_f32_16x16x128_f8f6f4 v[122:125], v[18:25], v[212:219], v[122:125]
	v_mfma_f32_16x16x128_f8f6f4 v[114:117], v[26:33], v[212:219], v[114:117]
	v_mfma_f32_16x16x128_f8f6f4 v[106:109], v[18:25], v[220:227], v[106:109]
	v_mfma_f32_16x16x128_f8f6f4 v[98:101], v[26:33], v[220:227], v[98:101]
	s_setprio 0
	s_barrier
	ds_read_b128 v[196:199], v183 offset:49152
	ds_read_b128 v[204:207], v183 offset:51200
	ds_read_b128 v[200:203], v184 offset:49152
	ds_read_b128 v[208:211], v184 offset:51200
	ds_read_b128 v[212:215], v183 offset:53248
	ds_read_b128 v[220:223], v183 offset:55296
	ds_read_b128 v[216:219], v184 offset:53248
	ds_read_b128 v[224:227], v184 offset:55296
	s_add_u32 s42, s69, 0x180
	s_addc_u32 s43, s70, 0
	s_mov_b32 m0, s55
	s_nop 0
	global_load_lds_dwordx4 v1, s[42:43] offset:0
	s_nop 0
	s_mov_b32 m0, s56
	s_nop 0
	global_load_lds_dwordx4 v173, s[42:43] offset:0
	s_add_u32 s42, s69, 0x20180
	s_addc_u32 s43, s70, 0
	s_mov_b32 m0, s59
	s_nop 0
	global_load_lds_dwordx4 v1, s[42:43] offset:0
	s_nop 0
	s_mov_b32 m0, s60
	s_nop 0
	global_load_lds_dwordx4 v173, s[42:43] offset:0
	s_add_u32 s42, s39, 0x180
	s_addc_u32 s43, s68, 0
	s_mov_b32 m0, s57
	s_nop 0
	global_load_lds_dwordx4 v171, s[42:43] offset:0
	s_nop 0
	s_mov_b32 m0, s58
	s_nop 0
	global_load_lds_dwordx4 v174, s[42:43] offset:0
	s_waitcnt vmcnt(8)
	s_waitcnt lgkmcnt(0)
	s_barrier
	s_setprio 1
	s_waitcnt lgkmcnt(5)
	v_mfma_f32_16x16x128_f8f6f4 v[94:97], v[2:9], v[196:203], v[94:97]
	v_mfma_f32_16x16x128_f8f6f4 v[86:89], v[10:17], v[196:203], v[86:89]
	s_waitcnt lgkmcnt(4)
	v_mfma_f32_16x16x128_f8f6f4 v[78:81], v[2:9], v[204:211], v[78:81]
	v_mfma_f32_16x16x128_f8f6f4 v[70:73], v[10:17], v[204:211], v[70:73]
	s_waitcnt lgkmcnt(1)
	v_mfma_f32_16x16x128_f8f6f4 v[62:65], v[2:9], v[212:219], v[62:65]
	v_mfma_f32_16x16x128_f8f6f4 v[54:57], v[10:17], v[212:219], v[54:57]
	s_waitcnt lgkmcnt(0)
	v_mfma_f32_16x16x128_f8f6f4 v[46:49], v[2:9], v[220:227], v[46:49]
	v_mfma_f32_16x16x128_f8f6f4 v[38:41], v[10:17], v[220:227], v[38:41]
	s_setprio 0
	s_setprio 1
	v_mfma_f32_16x16x128_f8f6f4 v[90:93], v[18:25], v[196:203], v[90:93]
	v_mfma_f32_16x16x128_f8f6f4 v[82:85], v[26:33], v[196:203], v[82:85]
	v_mfma_f32_16x16x128_f8f6f4 v[74:77], v[18:25], v[204:211], v[74:77]
	v_mfma_f32_16x16x128_f8f6f4 v[66:69], v[26:33], v[204:211], v[66:69]
	v_mfma_f32_16x16x128_f8f6f4 v[58:61], v[18:25], v[212:219], v[58:61]
	v_mfma_f32_16x16x128_f8f6f4 v[50:53], v[26:33], v[212:219], v[50:53]
	v_mfma_f32_16x16x128_f8f6f4 v[42:45], v[18:25], v[220:227], v[42:45]
	v_mfma_f32_16x16x128_f8f6f4 v[34:37], v[26:33], v[220:227], v[34:37]
	s_setprio 0
	s_add_i32 s35, s35, 2
	s_add_u32 s4, s4, 0x100
	s_addc_u32 s5, s5, 0
	s_cmp_lt_u32 s35, 4
	s_barrier
	s_cbranch_scc1 .LBB0_561
	ds_read_b128 v[18:21], v179
	ds_read_b128 v[26:29], v179 offset:2048
	ds_read_b128 v[22:25], v180
	ds_read_b128 v[30:33], v180 offset:2048
	ds_read_b128 v[2:5], v181
	ds_read_b128 v[10:13], v181 offset:2048
	ds_read_b128 v[6:9], v182
	ds_read_b128 v[14:17], v182 offset:2048
	ds_read_b128 v[196:199], v183
	ds_read_b128 v[204:207], v183 offset:2048
	ds_read_b128 v[200:203], v184
	ds_read_b128 v[208:211], v184 offset:2048
	ds_read_b128 v[212:215], v183 offset:4096
	ds_read_b128 v[220:223], v183 offset:6144
	ds_read_b128 v[216:219], v184 offset:4096
	ds_read_b128 v[224:227], v184 offset:6144
	s_mov_b32 m0, s61
	s_nop 0
	global_load_lds_dwordx4 v172, s[24:25] offset:0
	s_nop 0
	s_mov_b32 m0, s62
	s_nop 0
	global_load_lds_dwordx4 v175, s[24:25] offset:0
	s_waitcnt vmcnt(8)
	s_waitcnt lgkmcnt(0)
	s_barrier
	s_setprio 1
	s_waitcnt lgkmcnt(5)
	v_mfma_f32_16x16x128_f8f6f4 v[158:161], v[18:25], v[196:203], v[158:161]
	v_mfma_f32_16x16x128_f8f6f4 v[150:153], v[26:33], v[196:203], v[150:153]
	s_waitcnt lgkmcnt(4)
	v_mfma_f32_16x16x128_f8f6f4 v[142:145], v[18:25], v[204:211], v[142:145]
	v_mfma_f32_16x16x128_f8f6f4 v[134:137], v[26:33], v[204:211], v[134:137]
	s_waitcnt lgkmcnt(1)
	v_mfma_f32_16x16x128_f8f6f4 v[126:129], v[18:25], v[212:219], v[126:129]
	v_mfma_f32_16x16x128_f8f6f4 v[118:121], v[26:33], v[212:219], v[118:121]
	s_waitcnt lgkmcnt(0)
	v_mfma_f32_16x16x128_f8f6f4 v[110:113], v[18:25], v[220:227], v[110:113]
	v_mfma_f32_16x16x128_f8f6f4 v[102:105], v[26:33], v[220:227], v[102:105]
	s_setprio 0
	s_setprio 1
	v_mfma_f32_16x16x128_f8f6f4 v[154:157], v[2:9], v[196:203], v[154:157]
	v_mfma_f32_16x16x128_f8f6f4 v[146:149], v[10:17], v[196:203], v[146:149]
	v_mfma_f32_16x16x128_f8f6f4 v[138:141], v[2:9], v[204:211], v[138:141]
	v_mfma_f32_16x16x128_f8f6f4 v[130:133], v[10:17], v[204:211], v[130:133]
	v_mfma_f32_16x16x128_f8f6f4 v[122:125], v[2:9], v[212:219], v[122:125]
	v_mfma_f32_16x16x128_f8f6f4 v[114:117], v[10:17], v[212:219], v[114:117]
	v_mfma_f32_16x16x128_f8f6f4 v[106:109], v[2:9], v[220:227], v[106:109]
	v_mfma_f32_16x16x128_f8f6f4 v[98:101], v[10:17], v[220:227], v[98:101]
	s_setprio 0
	s_barrier
	v_cndmask_b32_e64 v196, 0, 1, s[46:47]
	v_cmp_ne_u32_e64 s[4:5], 1, v196
	s_andn2_b64 vcc, exec, s[46:47]
	s_cbranch_vccnz .LBB0_564
	v_mov_b32_e32 v171, v0
	s_lshl_b32 s35, s66, 9
	s_add_i32 s35, s35, 0
	v_lshrrev_b32_e32 v172, 4, v171
	v_xor_b32_e32 v172, v172, v171
	s_add_i32 s35, s35, 0x20480
	v_ashrrev_i32_e32 v174, 3, v171
	v_lshl_add_u32 v171, v171, 4, v170
	v_lshl_add_u32 v174, v174, 1, s35
	v_ashrrev_i32_e32 v171, 7, v171
	v_lshl_add_u32 v171, v171, 1, s35
	ds_read_u16 v175, v174
	ds_read_u16 v174, v174 offset:256
	ds_read_u16 v196, v171
	ds_read_u16 v197, v171 offset:256
	v_lshlrev_b32_e32 v172, 4, v172
	v_and_b32_e32 v198, 0x70, v172
	s_waitcnt lgkmcnt(3)
	v_lshl_or_b32 v171, v175, 10, v198
	s_waitcnt lgkmcnt(2)
	v_lshl_or_b32 v172, v174, 10, v198
	s_waitcnt lgkmcnt(1)
	v_lshl_or_b32 v174, v196, 10, v198
	s_waitcnt lgkmcnt(0)
	v_lshl_or_b32 v175, v197, 10, v198

.LBB0_649:
	s_mov_b32 s35, -2
	.p2align 6
	s_nop 0
	ds_read_b128 v[18:21], v176
	ds_read_b128 v[26:29], v176 offset:2048
	ds_read_b128 v[22:25], v177
	ds_read_b128 v[30:33], v177 offset:2048
	ds_read_b128 v[2:5], v178
	ds_read_b128 v[10:13], v178 offset:2048
	ds_read_b128 v[6:9], v179
	ds_read_b128 v[14:17], v179 offset:2048
	ds_read_b128 v[194:197], v180
	ds_read_b128 v[202:205], v180 offset:2048
	ds_read_b128 v[198:201], v181
	ds_read_b128 v[206:209], v181 offset:2048
	ds_read_b128 v[210:213], v180 offset:4096
	ds_read_b128 v[218:221], v180 offset:6144
	ds_read_b128 v[214:217], v181 offset:4096
	ds_read_b128 v[222:225], v181 offset:6144
	s_add_u32 s64, s12, s4
	s_addc_u32 s65, s13, s5
	s_add_u32 s46, s64, 0x80
	s_addc_u32 s47, s65, 0
	s_mov_b32 m0, s58
	s_nop 0
	global_load_lds_dwordx4 v163, s[46:47] offset:0
	s_nop 0
	s_mov_b32 m0, s59
	s_nop 0
	global_load_lds_dwordx4 v171, s[46:47] offset:0
	s_waitcnt vmcnt(8)
	s_waitcnt lgkmcnt(0)
	s_barrier
	s_setprio 1
	s_waitcnt lgkmcnt(0)
	v_mfma_f32_16x16x128_f8f6f4 v[158:161], v[18:25], v[194:201], 0
	v_mfma_f32_16x16x128_f8f6f4 v[154:157], v[26:33], v[194:201], 0
	v_mfma_f32_16x16x128_f8f6f4 v[142:145], v[18:25], v[202:209], 0
	v_mfma_f32_16x16x128_f8f6f4 v[138:141], v[26:33], v[202:209], 0
	v_mfma_f32_16x16x128_f8f6f4 v[126:129], v[18:25], v[210:217], 0
	v_mfma_f32_16x16x128_f8f6f4 v[122:125], v[26:33], v[210:217], 0
	v_mfma_f32_16x16x128_f8f6f4 v[110:113], v[18:25], v[218:225], 0
	v_mfma_f32_16x16x128_f8f6f4 v[106:109], v[26:33], v[218:225], 0
	s_setprio 0
	s_setprio 1
	v_mfma_f32_16x16x128_f8f6f4 v[150:153], v[2:9], v[194:201], 0
	v_mfma_f32_16x16x128_f8f6f4 v[146:149], v[10:17], v[194:201], 0
	v_mfma_f32_16x16x128_f8f6f4 v[134:137], v[2:9], v[202:209], 0
	v_mfma_f32_16x16x128_f8f6f4 v[130:133], v[10:17], v[202:209], 0
	v_mfma_f32_16x16x128_f8f6f4 v[118:121], v[2:9], v[210:217], 0
	v_mfma_f32_16x16x128_f8f6f4 v[114:117], v[10:17], v[210:217], 0
	v_mfma_f32_16x16x128_f8f6f4 v[102:105], v[2:9], v[218:225], 0
	v_mfma_f32_16x16x128_f8f6f4 v[98:101], v[10:17], v[218:225], 0
	s_setprio 0
	s_barrier
	s_add_u32 s66, s42, s4
	s_addc_u32 s67, s43, s5
	ds_read_b128 v[194:197], v180 offset:16384
	ds_read_b128 v[202:205], v180 offset:18432
	ds_read_b128 v[198:201], v181 offset:16384
	ds_read_b128 v[206:209], v181 offset:18432
	ds_read_b128 v[210:213], v180 offset:20480
	ds_read_b128 v[218:221], v180 offset:22528
	ds_read_b128 v[214:217], v181 offset:20480
	ds_read_b128 v[222:225], v181 offset:22528
	s_add_u32 s46, s66, 0x100
	s_addc_u32 s47, s67, 0
	s_mov_b32 m0, s33
	s_nop 0
	global_load_lds_dwordx4 v172, s[46:47] offset:0
	s_nop 0
	s_mov_b32 m0, s39
	s_nop 0
	global_load_lds_dwordx4 v173, s[46:47] offset:0
	s_add_u32 s46, s66, 0x20100
	s_addc_u32 s47, s67, 0
	s_mov_b32 m0, s41
	s_nop 0
	global_load_lds_dwordx4 v172, s[46:47] offset:0
	s_nop 0
	s_mov_b32 m0, s48
	s_nop 0
	global_load_lds_dwordx4 v173, s[46:47] offset:0
	s_add_u32 s46, s64, 0x100
	s_addc_u32 s47, s65, 0
	s_mov_b32 m0, s1
	s_nop 0
	global_load_lds_dwordx4 v162, s[46:47] offset:0
	s_nop 0
	s_mov_b32 m0, s49
	s_nop 0
	global_load_lds_dwordx4 v170, s[46:47] offset:0
	s_waitcnt vmcnt(8)
	s_waitcnt lgkmcnt(0)
	s_barrier
	s_setprio 1
	s_waitcnt lgkmcnt(5)
	v_mfma_f32_16x16x128_f8f6f4 v[94:97], v[18:25], v[194:201], 0
	v_mfma_f32_16x16x128_f8f6f4 v[90:93], v[26:33], v[194:201], 0
	s_waitcnt lgkmcnt(4)
	v_mfma_f32_16x16x128_f8f6f4 v[78:81], v[18:25], v[202:209], 0
	v_mfma_f32_16x16x128_f8f6f4 v[74:77], v[26:33], v[202:209], 0
	s_waitcnt lgkmcnt(1)
	v_mfma_f32_16x16x128_f8f6f4 v[62:65], v[18:25], v[210:217], 0
	v_mfma_f32_16x16x128_f8f6f4 v[58:61], v[26:33], v[210:217], 0
	s_waitcnt lgkmcnt(0)
	v_mfma_f32_16x16x128_f8f6f4 v[46:49], v[18:25], v[218:225], 0
	v_mfma_f32_16x16x128_f8f6f4 v[42:45], v[26:33], v[218:225], 0
	s_setprio 0
	s_setprio 1
	v_mfma_f32_16x16x128_f8f6f4 v[86:89], v[2:9], v[194:201], 0
	v_mfma_f32_16x16x128_f8f6f4 v[82:85], v[10:17], v[194:201], 0
	v_mfma_f32_16x16x128_f8f6f4 v[70:73], v[2:9], v[202:209], 0
	v_mfma_f32_16x16x128_f8f6f4 v[66:69], v[10:17], v[202:209], 0
	v_mfma_f32_16x16x128_f8f6f4 v[54:57], v[2:9], v[210:217], 0
	v_mfma_f32_16x16x128_f8f6f4 v[50:53], v[10:17], v[210:217], 0
	v_mfma_f32_16x16x128_f8f6f4 v[38:41], v[2:9], v[218:225], 0
	v_mfma_f32_16x16x128_f8f6f4 v[34:37], v[10:17], v[218:225], 0
	s_setprio 0
	s_barrier
	s_add_i32 s68, 0, 0x18000
	v_add_u32_e32 v183, s68, v174
	v_add_u32_e32 v184, s68, v175
	s_add_i32 s68, 0, 0x1c000
	v_add_u32_e32 v185, s68, v174
	ds_read_b128 v[2:5], v183
	ds_read_b128 v[10:13], v183 offset:2048
	ds_read_b128 v[6:9], v184
	ds_read_b128 v[14:17], v184 offset:2048
	v_add_u32_e32 v186, s68, v175
	ds_read_b128 v[18:21], v185
	ds_read_b128 v[26:29], v185 offset:2048
	ds_read_b128 v[22:25], v186
	ds_read_b128 v[30:33], v186 offset:2048
	ds_read_b128 v[194:197], v180 offset:32768
	ds_read_b128 v[202:205], v180 offset:34816
	ds_read_b128 v[198:201], v181 offset:32768
	ds_read_b128 v[206:209], v181 offset:34816
	ds_read_b128 v[210:213], v180 offset:36864
	ds_read_b128 v[218:221], v180 offset:38912
	ds_read_b128 v[214:217], v181 offset:36864
	ds_read_b128 v[222:225], v181 offset:38912
	s_mov_b32 m0, s50
	s_nop 0
	global_load_lds_dwordx4 v163, s[46:47] offset:0
	s_nop 0
	s_mov_b32 m0, s51
	s_nop 0
	global_load_lds_dwordx4 v171, s[46:47] offset:0
	s_waitcnt vmcnt(8)
	s_waitcnt lgkmcnt(0)
	s_barrier
	s_setprio 1
	s_waitcnt lgkmcnt(5)
	v_mfma_f32_16x16x128_f8f6f4 v[158:161], v[2:9], v[194:201], v[158:161]
	v_mfma_f32_16x16x128_f8f6f4 v[154:157], v[10:17], v[194:201], v[154:157]
	s_waitcnt lgkmcnt(4)
	v_mfma_f32_16x16x128_f8f6f4 v[142:145], v[2:9], v[202:209], v[142:145]
	v_mfma_f32_16x16x128_f8f6f4 v[138:141], v[10:17], v[202:209], v[138:141]
	s_waitcnt lgkmcnt(1)
	v_mfma_f32_16x16x128_f8f6f4 v[126:129], v[2:9], v[210:217], v[126:129]
	v_mfma_f32_16x16x128_f8f6f4 v[122:125], v[10:17], v[210:217], v[122:125]
	s_waitcnt lgkmcnt(0)
	v_mfma_f32_16x16x128_f8f6f4 v[110:113], v[2:9], v[218:225], v[110:113]
	v_mfma_f32_16x16x128_f8f6f4 v[106:109], v[10:17], v[218:225], v[106:109]
	s_setprio 0
	s_setprio 1
	v_mfma_f32_16x16x128_f8f6f4 v[150:153], v[18:25], v[194:201], v[150:153]
	v_mfma_f32_16x16x128_f8f6f4 v[146:149], v[26:33], v[194:201], v[146:149]
	v_mfma_f32_16x16x128_f8f6f4 v[134:137], v[18:25], v[202:209], v[134:137]
	v_mfma_f32_16x16x128_f8f6f4 v[130:133], v[26:33], v[202:209], v[130:133]
	v_mfma_f32_16x16x128_f8f6f4 v[118:121], v[18:25], v[210:217], v[118:121]
	v_mfma_f32_16x16x128_f8f6f4 v[114:117], v[26:33], v[210:217], v[114:117]
	v_mfma_f32_16x16x128_f8f6f4 v[102:105], v[18:25], v[218:225], v[102:105]
	v_mfma_f32_16x16x128_f8f6f4 v[98:101], v[26:33], v[218:225], v[98:101]
	s_setprio 0
	s_barrier
	ds_read_b128 v[194:197], v180 offset:49152
	ds_read_b128 v[202:205], v180 offset:51200
	ds_read_b128 v[198:201], v181 offset:49152
	ds_read_b128 v[206:209], v181 offset:51200
	ds_read_b128 v[210:213], v180 offset:53248
	ds_read_b128 v[218:221], v180 offset:55296
	ds_read_b128 v[214:217], v181 offset:53248
	ds_read_b128 v[222:225], v181 offset:55296
	s_add_u32 s46, s66, 0x180
	s_addc_u32 s47, s67, 0
	s_mov_b32 m0, s52
	s_nop 0
	global_load_lds_dwordx4 v172, s[46:47] offset:0
	s_nop 0
	s_mov_b32 m0, s53
	s_nop 0
	global_load_lds_dwordx4 v173, s[46:47] offset:0
	s_add_u32 s46, s66, 0x20180
	s_addc_u32 s47, s67, 0
	s_mov_b32 m0, s56
	s_nop 0
	global_load_lds_dwordx4 v172, s[46:47] offset:0
	s_nop 0
	s_mov_b32 m0, s57
	s_nop 0
	global_load_lds_dwordx4 v173, s[46:47] offset:0
	s_add_u32 s46, s64, 0x180
	s_addc_u32 s47, s65, 0
	s_mov_b32 m0, s54
	s_nop 0
	global_load_lds_dwordx4 v162, s[46:47] offset:0
	s_nop 0
	s_mov_b32 m0, s55
	s_nop 0
	global_load_lds_dwordx4 v170, s[46:47] offset:0
	s_waitcnt vmcnt(8)
	s_waitcnt lgkmcnt(0)
	s_barrier
	s_setprio 1
	s_waitcnt lgkmcnt(5)
	v_mfma_f32_16x16x128_f8f6f4 v[94:97], v[2:9], v[194:201], v[94:97]
	v_mfma_f32_16x16x128_f8f6f4 v[90:93], v[10:17], v[194:201], v[90:93]
	s_waitcnt lgkmcnt(4)
	v_mfma_f32_16x16x128_f8f6f4 v[78:81], v[2:9], v[202:209], v[78:81]
	v_mfma_f32_16x16x128_f8f6f4 v[74:77], v[10:17], v[202:209], v[74:77]
	s_waitcnt lgkmcnt(1)
	v_mfma_f32_16x16x128_f8f6f4 v[62:65], v[2:9], v[210:217], v[62:65]
	v_mfma_f32_16x16x128_f8f6f4 v[58:61], v[10:17], v[210:217], v[58:61]
	s_waitcnt lgkmcnt(0)
	v_mfma_f32_16x16x128_f8f6f4 v[46:49], v[2:9], v[218:225], v[46:49]
	v_mfma_f32_16x16x128_f8f6f4 v[42:45], v[10:17], v[218:225], v[42:45]
	s_setprio 0
	s_setprio 1
	v_mfma_f32_16x16x128_f8f6f4 v[86:89], v[18:25], v[194:201], v[86:89]
	v_mfma_f32_16x16x128_f8f6f4 v[82:85], v[26:33], v[194:201], v[82:85]
	v_mfma_f32_16x16x128_f8f6f4 v[70:73], v[18:25], v[202:209], v[70:73]
	v_mfma_f32_16x16x128_f8f6f4 v[66:69], v[26:33], v[202:209], v[66:69]
	v_mfma_f32_16x16x128_f8f6f4 v[54:57], v[18:25], v[210:217], v[54:57]
	v_mfma_f32_16x16x128_f8f6f4 v[50:53], v[26:33], v[210:217], v[50:53]
	v_mfma_f32_16x16x128_f8f6f4 v[38:41], v[18:25], v[218:225], v[38:41]
	v_mfma_f32_16x16x128_f8f6f4 v[34:37], v[26:33], v[218:225], v[34:37]
	s_setprio 0
	s_add_i32 s35, s35, 2
	s_add_u32 s4, s4, 0x100
	s_addc_u32 s5, s5, 0
	s_barrier
.LBB0_650:
	.p2align 6
	s_nop 0
	ds_read_b128 v[18:21], v176
	ds_read_b128 v[26:29], v176 offset:2048
	ds_read_b128 v[22:25], v177
	ds_read_b128 v[30:33], v177 offset:2048
	ds_read_b128 v[2:5], v178
	ds_read_b128 v[10:13], v178 offset:2048
	ds_read_b128 v[6:9], v179
	ds_read_b128 v[14:17], v179 offset:2048
	ds_read_b128 v[194:197], v180
	ds_read_b128 v[202:205], v180 offset:2048
	ds_read_b128 v[198:201], v181
	ds_read_b128 v[206:209], v181 offset:2048
	ds_read_b128 v[210:213], v180 offset:4096
	ds_read_b128 v[218:221], v180 offset:6144
	ds_read_b128 v[214:217], v181 offset:4096
	ds_read_b128 v[222:225], v181 offset:6144
	s_add_u32 s64, s12, s4
	s_addc_u32 s65, s13, s5
	s_add_u32 s46, s64, 0x80
	s_addc_u32 s47, s65, 0
	s_mov_b32 m0, s58
	s_nop 0
	global_load_lds_dwordx4 v163, s[46:47] offset:0
	s_nop 0
	s_mov_b32 m0, s59
	s_nop 0
	global_load_lds_dwordx4 v171, s[46:47] offset:0
	s_waitcnt vmcnt(8)
	s_waitcnt lgkmcnt(0)
	s_barrier
	s_setprio 1
	s_waitcnt lgkmcnt(0)
	v_mfma_f32_16x16x128_f8f6f4 v[158:161], v[18:25], v[194:201], v[158:161]
	v_mfma_f32_16x16x128_f8f6f4 v[154:157], v[26:33], v[194:201], v[154:157]
	v_mfma_f32_16x16x128_f8f6f4 v[142:145], v[18:25], v[202:209], v[142:145]
	v_mfma_f32_16x16x128_f8f6f4 v[138:141], v[26:33], v[202:209], v[138:141]
	v_mfma_f32_16x16x128_f8f6f4 v[126:129], v[18:25], v[210:217], v[126:129]
	v_mfma_f32_16x16x128_f8f6f4 v[122:125], v[26:33], v[210:217], v[122:125]
	v_mfma_f32_16x16x128_f8f6f4 v[110:113], v[18:25], v[218:225], v[110:113]
	v_mfma_f32_16x16x128_f8f6f4 v[106:109], v[26:33], v[218:225], v[106:109]
	s_setprio 0
	s_setprio 1
	v_mfma_f32_16x16x128_f8f6f4 v[150:153], v[2:9], v[194:201], v[150:153]
	v_mfma_f32_16x16x128_f8f6f4 v[146:149], v[10:17], v[194:201], v[146:149]
	v_mfma_f32_16x16x128_f8f6f4 v[134:137], v[2:9], v[202:209], v[134:137]
	v_mfma_f32_16x16x128_f8f6f4 v[130:133], v[10:17], v[202:209], v[130:133]
	v_mfma_f32_16x16x128_f8f6f4 v[118:121], v[2:9], v[210:217], v[118:121]
	v_mfma_f32_16x16x128_f8f6f4 v[114:117], v[10:17], v[210:217], v[114:117]
	v_mfma_f32_16x16x128_f8f6f4 v[102:105], v[2:9], v[218:225], v[102:105]
	v_mfma_f32_16x16x128_f8f6f4 v[98:101], v[10:17], v[218:225], v[98:101]
	s_setprio 0
	s_barrier
	s_add_u32 s66, s42, s4
	s_addc_u32 s67, s43, s5
	ds_read_b128 v[194:197], v180 offset:16384
	ds_read_b128 v[202:205], v180 offset:18432
	ds_read_b128 v[198:201], v181 offset:16384
	ds_read_b128 v[206:209], v181 offset:18432
	ds_read_b128 v[210:213], v180 offset:20480
	ds_read_b128 v[218:221], v180 offset:22528
	ds_read_b128 v[214:217], v181 offset:20480
	ds_read_b128 v[222:225], v181 offset:22528
	s_add_u32 s46, s66, 0x100
	s_addc_u32 s47, s67, 0
	s_mov_b32 m0, s33
	s_nop 0
	global_load_lds_dwordx4 v172, s[46:47] offset:0
	s_nop 0
	s_mov_b32 m0, s39
	s_nop 0
	global_load_lds_dwordx4 v173, s[46:47] offset:0
	s_add_u32 s46, s66, 0x20100
	s_addc_u32 s47, s67, 0
	s_mov_b32 m0, s41
	s_nop 0
	global_load_lds_dwordx4 v172, s[46:47] offset:0
	s_nop 0
	s_mov_b32 m0, s48
	s_nop 0
	global_load_lds_dwordx4 v173, s[46:47] offset:0
	s_add_u32 s46, s64, 0x100
	s_addc_u32 s47, s65, 0
	s_mov_b32 m0, s1
	s_nop 0
	global_load_lds_dwordx4 v162, s[46:47] offset:0
	s_nop 0
	s_mov_b32 m0, s49
	s_nop 0
	global_load_lds_dwordx4 v170, s[46:47] offset:0
	s_waitcnt vmcnt(8)
	s_waitcnt lgkmcnt(0)
	s_barrier
	s_setprio 1
	s_waitcnt lgkmcnt(5)
	v_mfma_f32_16x16x128_f8f6f4 v[94:97], v[18:25], v[194:201], v[94:97]
	v_mfma_f32_16x16x128_f8f6f4 v[90:93], v[26:33], v[194:201], v[90:93]
	s_waitcnt lgkmcnt(4)
	v_mfma_f32_16x16x128_f8f6f4 v[78:81], v[18:25], v[202:209], v[78:81]
	v_mfma_f32_16x16x128_f8f6f4 v[74:77], v[26:33], v[202:209], v[74:77]
	s_waitcnt lgkmcnt(1)
	v_mfma_f32_16x16x128_f8f6f4 v[62:65], v[18:25], v[210:217], v[62:65]
	v_mfma_f32_16x16x128_f8f6f4 v[58:61], v[26:33], v[210:217], v[58:61]
	s_waitcnt lgkmcnt(0)
	v_mfma_f32_16x16x128_f8f6f4 v[46:49], v[18:25], v[218:225], v[46:49]
	v_mfma_f32_16x16x128_f8f6f4 v[42:45], v[26:33], v[218:225], v[42:45]
	s_setprio 0
	s_setprio 1
	v_mfma_f32_16x16x128_f8f6f4 v[86:89], v[2:9], v[194:201], v[86:89]
	v_mfma_f32_16x16x128_f8f6f4 v[82:85], v[10:17], v[194:201], v[82:85]
	v_mfma_f32_16x16x128_f8f6f4 v[70:73], v[2:9], v[202:209], v[70:73]
	v_mfma_f32_16x16x128_f8f6f4 v[66:69], v[10:17], v[202:209], v[66:69]
	v_mfma_f32_16x16x128_f8f6f4 v[54:57], v[2:9], v[210:217], v[54:57]
	v_mfma_f32_16x16x128_f8f6f4 v[50:53], v[10:17], v[210:217], v[50:53]
	v_mfma_f32_16x16x128_f8f6f4 v[38:41], v[2:9], v[218:225], v[38:41]
	v_mfma_f32_16x16x128_f8f6f4 v[34:37], v[10:17], v[218:225], v[34:37]
	s_setprio 0
	s_barrier
	s_add_i32 s68, 0, 0x18000
	v_add_u32_e32 v183, s68, v174
	v_add_u32_e32 v184, s68, v175
	s_add_i32 s68, 0, 0x1c000
	v_add_u32_e32 v185, s68, v174
	ds_read_b128 v[2:5], v183
	ds_read_b128 v[10:13], v183 offset:2048
	ds_read_b128 v[6:9], v184
	ds_read_b128 v[14:17], v184 offset:2048
	v_add_u32_e32 v186, s68, v175
	ds_read_b128 v[18:21], v185
	ds_read_b128 v[26:29], v185 offset:2048
	ds_read_b128 v[22:25], v186
	ds_read_b128 v[30:33], v186 offset:2048
	ds_read_b128 v[194:197], v180 offset:32768
	ds_read_b128 v[202:205], v180 offset:34816
	ds_read_b128 v[198:201], v181 offset:32768
	ds_read_b128 v[206:209], v181 offset:34816
	ds_read_b128 v[210:213], v180 offset:36864
	ds_read_b128 v[218:221], v180 offset:38912
	ds_read_b128 v[214:217], v181 offset:36864
	ds_read_b128 v[222:225], v181 offset:38912
	s_mov_b32 m0, s50
	s_nop 0
	global_load_lds_dwordx4 v163, s[46:47] offset:0
	s_nop 0
	s_mov_b32 m0, s51
	s_nop 0
	global_load_lds_dwordx4 v171, s[46:47] offset:0
	s_waitcnt vmcnt(8)
	s_waitcnt lgkmcnt(0)
	s_barrier
	s_setprio 1
	s_waitcnt lgkmcnt(5)
	v_mfma_f32_16x16x128_f8f6f4 v[158:161], v[2:9], v[194:201], v[158:161]
	v_mfma_f32_16x16x128_f8f6f4 v[154:157], v[10:17], v[194:201], v[154:157]
	s_waitcnt lgkmcnt(4)
	v_mfma_f32_16x16x128_f8f6f4 v[142:145], v[2:9], v[202:209], v[142:145]
	v_mfma_f32_16x16x128_f8f6f4 v[138:141], v[10:17], v[202:209], v[138:141]
	s_waitcnt lgkmcnt(1)
	v_mfma_f32_16x16x128_f8f6f4 v[126:129], v[2:9], v[210:217], v[126:129]
	v_mfma_f32_16x16x128_f8f6f4 v[122:125], v[10:17], v[210:217], v[122:125]
	s_waitcnt lgkmcnt(0)
	v_mfma_f32_16x16x128_f8f6f4 v[110:113], v[2:9], v[218:225], v[110:113]
	v_mfma_f32_16x16x128_f8f6f4 v[106:109], v[10:17], v[218:225], v[106:109]
	s_setprio 0
	s_setprio 1
	v_mfma_f32_16x16x128_f8f6f4 v[150:153], v[18:25], v[194:201], v[150:153]
	v_mfma_f32_16x16x128_f8f6f4 v[146:149], v[26:33], v[194:201], v[146:149]
	v_mfma_f32_16x16x128_f8f6f4 v[134:137], v[18:25], v[202:209], v[134:137]
	v_mfma_f32_16x16x128_f8f6f4 v[130:133], v[26:33], v[202:209], v[130:133]
	v_mfma_f32_16x16x128_f8f6f4 v[118:121], v[18:25], v[210:217], v[118:121]
	v_mfma_f32_16x16x128_f8f6f4 v[114:117], v[26:33], v[210:217], v[114:117]
	v_mfma_f32_16x16x128_f8f6f4 v[102:105], v[18:25], v[218:225], v[102:105]
	v_mfma_f32_16x16x128_f8f6f4 v[98:101], v[26:33], v[218:225], v[98:101]
	s_setprio 0
	s_barrier
	ds_read_b128 v[194:197], v180 offset:49152
	ds_read_b128 v[202:205], v180 offset:51200
	ds_read_b128 v[198:201], v181 offset:49152
	ds_read_b128 v[206:209], v181 offset:51200
	ds_read_b128 v[210:213], v180 offset:53248
	ds_read_b128 v[218:221], v180 offset:55296
	ds_read_b128 v[214:217], v181 offset:53248
	ds_read_b128 v[222:225], v181 offset:55296
	s_add_u32 s46, s66, 0x180
	s_addc_u32 s47, s67, 0
	s_mov_b32 m0, s52
	s_nop 0
	global_load_lds_dwordx4 v172, s[46:47] offset:0
	s_nop 0
	s_mov_b32 m0, s53
	s_nop 0
	global_load_lds_dwordx4 v173, s[46:47] offset:0
	s_add_u32 s46, s66, 0x20180
	s_addc_u32 s47, s67, 0
	s_mov_b32 m0, s56
	s_nop 0
	global_load_lds_dwordx4 v172, s[46:47] offset:0
	s_nop 0
	s_mov_b32 m0, s57
	s_nop 0
	global_load_lds_dwordx4 v173, s[46:47] offset:0
	s_add_u32 s46, s64, 0x180
	s_addc_u32 s47, s65, 0
	s_mov_b32 m0, s54
	s_nop 0
	global_load_lds_dwordx4 v162, s[46:47] offset:0
	s_nop 0
	s_mov_b32 m0, s55
	s_nop 0
	global_load_lds_dwordx4 v170, s[46:47] offset:0
	s_waitcnt vmcnt(8)
	s_waitcnt lgkmcnt(0)
	s_barrier
	s_setprio 1
	s_waitcnt lgkmcnt(5)
	v_mfma_f32_16x16x128_f8f6f4 v[94:97], v[2:9], v[194:201], v[94:97]
	v_mfma_f32_16x16x128_f8f6f4 v[90:93], v[10:17], v[194:201], v[90:93]
	s_waitcnt lgkmcnt(4)
	v_mfma_f32_16x16x128_f8f6f4 v[78:81], v[2:9], v[202:209], v[78:81]
	v_mfma_f32_16x16x128_f8f6f4 v[74:77], v[10:17], v[202:209], v[74:77]
	s_waitcnt lgkmcnt(1)
	v_mfma_f32_16x16x128_f8f6f4 v[62:65], v[2:9], v[210:217], v[62:65]
	v_mfma_f32_16x16x128_f8f6f4 v[58:61], v[10:17], v[210:217], v[58:61]
	s_waitcnt lgkmcnt(0)
	v_mfma_f32_16x16x128_f8f6f4 v[46:49], v[2:9], v[218:225], v[46:49]
	v_mfma_f32_16x16x128_f8f6f4 v[42:45], v[10:17], v[218:225], v[42:45]
	s_setprio 0
	s_setprio 1
	v_mfma_f32_16x16x128_f8f6f4 v[86:89], v[18:25], v[194:201], v[86:89]
	v_mfma_f32_16x16x128_f8f6f4 v[82:85], v[26:33], v[194:201], v[82:85]
	v_mfma_f32_16x16x128_f8f6f4 v[70:73], v[18:25], v[202:209], v[70:73]
	v_mfma_f32_16x16x128_f8f6f4 v[66:69], v[26:33], v[202:209], v[66:69]
	v_mfma_f32_16x16x128_f8f6f4 v[54:57], v[18:25], v[210:217], v[54:57]
	v_mfma_f32_16x16x128_f8f6f4 v[50:53], v[26:33], v[210:217], v[50:53]
	v_mfma_f32_16x16x128_f8f6f4 v[38:41], v[18:25], v[218:225], v[38:41]
	v_mfma_f32_16x16x128_f8f6f4 v[34:37], v[26:33], v[218:225], v[34:37]
	s_setprio 0
	s_add_i32 s35, s35, 2
	s_add_u32 s4, s4, 0x100
	s_addc_u32 s5, s5, 0
	s_cmp_lt_u32 s35, 4
	s_barrier
	s_cbranch_scc1 .LBB0_650
	ds_read_b128 v[18:21], v176
	ds_read_b128 v[26:29], v176 offset:2048
	ds_read_b128 v[22:25], v177
	ds_read_b128 v[30:33], v177 offset:2048
	ds_read_b128 v[2:5], v178
	ds_read_b128 v[10:13], v178 offset:2048
	ds_read_b128 v[6:9], v179
	ds_read_b128 v[14:17], v179 offset:2048
	ds_read_b128 v[194:197], v180
	ds_read_b128 v[202:205], v180 offset:2048
	ds_read_b128 v[198:201], v181
	ds_read_b128 v[206:209], v181 offset:2048
	ds_read_b128 v[210:213], v180 offset:4096
	ds_read_b128 v[218:221], v180 offset:6144
	ds_read_b128 v[214:217], v181 offset:4096
	ds_read_b128 v[222:225], v181 offset:6144
	s_mov_b32 m0, s58
	s_nop 0
	global_load_lds_dwordx4 v163, s[24:25] offset:0
	s_nop 0
	s_mov_b32 m0, s59
	s_nop 0
	global_load_lds_dwordx4 v171, s[24:25] offset:0
	s_waitcnt vmcnt(8)
	s_waitcnt lgkmcnt(0)
	s_barrier
	s_setprio 1
	s_waitcnt lgkmcnt(5)
	v_mfma_f32_16x16x128_f8f6f4 v[158:161], v[18:25], v[194:201], v[158:161]
	v_mfma_f32_16x16x128_f8f6f4 v[154:157], v[26:33], v[194:201], v[154:157]
	s_waitcnt lgkmcnt(4)
	v_mfma_f32_16x16x128_f8f6f4 v[142:145], v[18:25], v[202:209], v[142:145]
	v_mfma_f32_16x16x128_f8f6f4 v[138:141], v[26:33], v[202:209], v[138:141]
	s_waitcnt lgkmcnt(1)
	v_mfma_f32_16x16x128_f8f6f4 v[126:129], v[18:25], v[210:217], v[126:129]
	v_mfma_f32_16x16x128_f8f6f4 v[122:125], v[26:33], v[210:217], v[122:125]
	s_waitcnt lgkmcnt(0)
	v_mfma_f32_16x16x128_f8f6f4 v[110:113], v[18:25], v[218:225], v[110:113]
	v_mfma_f32_16x16x128_f8f6f4 v[106:109], v[26:33], v[218:225], v[106:109]
	s_setprio 0
	s_setprio 1
	v_mfma_f32_16x16x128_f8f6f4 v[150:153], v[2:9], v[194:201], v[150:153]
	v_mfma_f32_16x16x128_f8f6f4 v[146:149], v[10:17], v[194:201], v[146:149]
	v_mfma_f32_16x16x128_f8f6f4 v[134:137], v[2:9], v[202:209], v[134:137]
	v_mfma_f32_16x16x128_f8f6f4 v[130:133], v[10:17], v[202:209], v[130:133]
	v_mfma_f32_16x16x128_f8f6f4 v[118:121], v[2:9], v[210:217], v[118:121]
	v_mfma_f32_16x16x128_f8f6f4 v[114:117], v[10:17], v[210:217], v[114:117]
	v_mfma_f32_16x16x128_f8f6f4 v[102:105], v[2:9], v[218:225], v[102:105]
	v_mfma_f32_16x16x128_f8f6f4 v[98:101], v[10:17], v[218:225], v[98:101]
	s_setprio 0
	s_barrier
	v_cndmask_b32_e64 v187, 0, 1, s[44:45]
	v_cmp_ne_u32_e64 s[4:5], 1, v187
	s_andn2_b64 vcc, exec, s[44:45]
	s_cbranch_vccnz .LBB0_653
	v_mov_b32_e32 v162, v0
	s_nop 0
	v_lshlrev_b32_e32 v163, 4, v162
	v_bitop3_b32 v163, v163, s0, v162 bitop3:0x48
	v_lshlrev_b32_e32 v162, 7, v162
	v_lshl_or_b32 v163, s61, 18, v163
	v_and_b32_e32 v162, 0xfffffc00, v162
	v_add_u32_e32 v162, v163, v162
	v_add_u32_e32 v163, 0x20000, v162
	v_add_u32_e32 v170, 0x10000, v162
	v_add_u32_e32 v171, 0x30000, v162
